# remaining plain epilogue stores write-through (in-projection extras, sums of squares, f32 output rows); no L2 write-back at any barrier of the layer loop
# baseline (speedup 1.0000x reference)
;     __device__ __forceinline__ void operator()(const Acc& acc, const Unit& u, int wr, int wc, int fr, int fq, const LAS float* tab) const {
;     ...
;                     for (int bj = 0; bj < 2; ++bj) rb[ai][m][bj] = *(const u32x4*)(xb + ((size_t)u.pm * BM + ai * HALF + wr * 64 + m * 16 + fr) * D + col0 + bj * HALF);
;             asm volatile("" : "+v"(rb[0][0][0]), "+v"(rb[0][0][1]), "+v"(rb[0][1][0]), "+v"(rb[0][1][1]), "+v"(rb[0][2][0]), "+v"(rb[0][2][1]), "+v"(rb[0][3][0]), "+v"(rb[0][3][1]),
;                              "+v"(rb[1][0][0]), "+v"(rb[1][0][1]), "+v"(rb[1][1][0]), "+v"(rb[1][1][1]), "+v"(rb[1][2][0]), "+v"(rb[1][2][1]), "+v"(rb[1][3][0]), "+v"(rb[1][3][1]));
;         }
; #pragma unroll
;         for (int ai = 0; ai < 2; ++ai)
; #pragma unroll
;             for (int m = 0; m < 4; ++m) {
;                 const size_t row = (size_t)u.pm * BM + ai * HALF + wr * 64 + m * 16 + fr; const size_t off = row * D + col0; float ss = 0.f;
; #pragma unroll
;                 for (int bj = 0; bj < 2; ++bj) { f32x4 b0, b1;
;                     if (base32) { b0 = __builtin_nontemporal_load((const f32x4*)(base32 + off + bj * HALF)); b1 = __builtin_nontemporal_load((const f32x4*)(base32 + off + bj * HALF + 4)); }
;                     else { const u32x4 b4 = rb[ai][m][bj];
;                         b0 = (f32x4){__uint_as_float(b4.x << 16), __uint_as_float(b4.x & 0xFFFF0000u), __uint_as_float(b4.y << 16), __uint_as_float(b4.y & 0xFFFF0000u)};
;                         b1 = (f32x4){__uint_as_float(b4.z << 16), __uint_as_float(b4.z & 0xFFFF0000u), __uint_as_float(b4.w << 16), __uint_as_float(b4.w & 0xFFFF0000u)}; }
;                     const f32x4 o0 = b0 + acc[ai][bj][m][0], o1 = b1 + acc[ai][bj][m][1];
;                     if (out32) {
;                         if (!dry) { *(f32x4*)(out32 + off + bj * HALF) = o0; *(f32x4*)(out32 + off + bj * HALF + 4) = o1; }
;                         continue; }
;                     ss += ((o0[0] * o0[0] + o0[1] * o0[1]) + (o0[2] * o0[2] + o0[3] * o0[3])) + ((o1[0] * o1[0] + o1[1] * o1[1]) + (o1[2] * o1[2] + o1[3] * o1[3]));
;                     u32x4 w; w.x = cvt_pk_bf16(o0[0], o0[1]); w.y = cvt_pk_bf16(o0[2], o0[3]); w.z = cvt_pk_bf16(o1[0], o1[1]); w.w = cvt_pk_bf16(o1[2], o1[3]);
;                     if (!dry) st16_wt(xb + off + bj * HALF, w); }
;                 if (out32) continue;
.LBB0_438:
	v_lshl_or_b32 v206, s22, 8, v213
	s_ashr_i32 s25, s24, 31
	s_lshl_b64 s[0:1], s[24:25], 8
	v_ashrrev_i32_e32 v207, 31, v206
	v_lshl_add_u64 v[208:209], s[0:1], 0, v[196:197]
	v_lshlrev_b64 v[210:211], 1, v[206:207]
	v_lshl_add_u64 v[98:99], s[10:11], 0, v[210:211]
	v_lshlrev_b64 v[220:221], 11, v[208:209]
	v_lshl_add_u64 v[98:99], v[98:99], 0, v[220:221]
	v_add_co_u32_e32 v100, vcc, 0x8000, v98
	global_load_dwordx4 v[216:219], v[98:99], off
	global_load_dwordx4 v[186:189], v[98:99], off offset:256
	v_addc_co_u32_e32 v101, vcc, 0, v99, vcc
	global_load_dwordx4 v[182:185], v[100:101], off
	global_load_dwordx4 v[178:181], v[100:101], off offset:256
	v_add_co_u32_e32 v100, vcc, 0x10000, v98
	v_lshl_add_u64 v[220:221], s[10:11], 0, v[220:221]
	s_nop 0
	v_addc_co_u32_e32 v101, vcc, 0, v99, vcc
	global_load_dwordx4 v[174:177], v[100:101], off
	global_load_dwordx4 v[170:173], v[100:101], off offset:256
	v_add_co_u32_e32 v100, vcc, 0x18000, v98
	v_lshl_add_u64 v[210:211], v[220:221], 0, v[210:211]
	s_nop 0
	v_addc_co_u32_e32 v101, vcc, 0, v99, vcc
	global_load_dwordx4 v[166:169], v[100:101], off
	global_load_dwordx4 v[162:165], v[100:101], off offset:256
	v_add_co_u32_e32 v100, vcc, 0x40000, v98
	s_lshl_b32 s0, s22, 2
	s_nop 0
	v_addc_co_u32_e32 v101, vcc, 0, v99, vcc
	global_load_dwordx4 v[158:161], v[100:101], off
	global_load_dwordx4 v[146:149], v[100:101], off offset:256
	v_add_co_u32_e32 v100, vcc, 0x48000, v98
	s_ashr_i32 s1, s0, 31
	s_nop 0
	v_addc_co_u32_e32 v101, vcc, 0, v99, vcc
	global_load_dwordx4 v[142:145], v[100:101], off
	global_load_dwordx4 v[138:141], v[100:101], off offset:256
	v_add_co_u32_e32 v100, vcc, 0x50000, v98
	s_lshl_b64 s[0:1], s[0:1], 2
	s_nop 0
	v_addc_co_u32_e32 v101, vcc, 0, v99, vcc
	v_add_co_u32_e32 v98, vcc, 0x58000, v98
	global_load_dwordx4 v[134:137], v[100:101], off
	global_load_dwordx4 v[122:125], v[100:101], off offset:256
	v_addc_co_u32_e32 v99, vcc, 0, v99, vcc
	global_load_dwordx4 v[110:113], v[98:99], off
	s_nop 0
	global_load_dwordx4 v[98:101], v[98:99], off offset:256
	s_add_u32 s22, s46, s0
	s_addc_u32 s23, s47, s1
	s_mov_b64 s[0:1], 0x100
	s_waitcnt vmcnt(0)
	s_nop 0
	v_lshlrev_b32_e32 v220, 16, v216
	v_and_b32_e32 v221, 0xffff0000, v216
	v_lshlrev_b32_e32 v216, 16, v217
	v_and_b32_e32 v217, 0xffff0000, v217
	v_lshlrev_b32_e32 v222, 16, v218
	v_and_b32_e32 v223, 0xffff0000, v218
	v_lshlrev_b32_e32 v218, 16, v219
	v_and_b32_e32 v219, 0xffff0000, v219
	v_pk_add_f32 v[156:157], v[156:157], v[216:217]
	v_pk_add_f32 v[154:155], v[154:155], v[220:221]
	v_pk_add_f32 v[216:217], v[152:153], v[218:219]
	v_pk_add_f32 v[152:153], v[150:151], v[222:223]
	v_mul_f32_e32 v150, v155, v155
	v_mul_f32_e32 v151, v157, v157
	v_fmac_f32_e32 v150, v154, v154
	v_fmac_f32_e32 v151, v156, v156
	v_add_f32_e32 v150, v150, v151
	v_mul_f32_e32 v151, v153, v153
	v_mul_f32_e32 v215, v217, v217
	v_fmac_f32_e32 v151, v152, v152
	v_fmac_f32_e32 v215, v216, v216
	v_add_f32_e32 v151, v151, v215
	v_add_f32_e32 v215, v150, v151
	v_cvt_pk_bf16_f32 v150, v154, v155
	v_cvt_pk_bf16_f32 v151, v156, v157
	v_cvt_pk_bf16_f32 v152, v152, v153
	v_cvt_pk_bf16_f32 v153, v216, v217
	v_lshlrev_b32_e32 v154, 16, v188
	global_store_dwordx4 v[210:211], v[150:153], off sc1
	s_nop 1
	v_lshlrev_b32_e32 v150, 16, v186
	v_and_b32_e32 v151, 0xffff0000, v186
	v_lshlrev_b32_e32 v152, 16, v187
	v_and_b32_e32 v153, 0xffff0000, v187
	v_and_b32_e32 v155, 0xffff0000, v188
	v_lshlrev_b32_e32 v156, 16, v189
	v_and_b32_e32 v157, 0xffff0000, v189
	v_pk_add_f32 v[132:133], v[132:133], v[152:153]
	v_pk_add_f32 v[130:131], v[130:131], v[150:151]
	v_pk_add_f32 v[150:151], v[128:129], v[156:157]
	v_pk_add_f32 v[128:129], v[126:127], v[154:155]
	v_mul_f32_e32 v126, v131, v131
	v_mul_f32_e32 v127, v133, v133
	v_fmac_f32_e32 v126, v130, v130
	v_fmac_f32_e32 v127, v132, v132
	v_add_f32_e32 v126, v126, v127
	v_mul_f32_e32 v127, v129, v129
	v_mul_f32_e32 v152, v151, v151
	v_fmac_f32_e32 v127, v128, v128
	v_fmac_f32_e32 v152, v150, v150
	v_add_f32_e32 v127, v127, v152
	v_add_f32_e32 v126, v126, v127
	v_add_f32_e32 v152, v215, v126
	v_cvt_pk_bf16_f32 v126, v130, v131
	v_cvt_pk_bf16_f32 v127, v132, v133
	v_cvt_pk_bf16_f32 v128, v128, v129
	v_cvt_pk_bf16_f32 v129, v150, v151
	v_lshl_add_u64 v[130:131], v[210:211], 0, s[0:1]
	global_store_dwordx4 v[130:131], v[126:129], off sc1
	s_nop 1
	v_mov_b32_e32 v126, v152
	s_nop 1
	v_permlane16_swap_b32_e32 v152, v126
	v_add_f32_e32 v126, v152, v126
	v_mov_b32_e32 v127, v126
	s_nop 1
	v_permlane32_swap_b32_e32 v126, v127
	s_and_saveexec_b64 s[24:25], s[4:5]
	s_cbranch_execz .LBB0_440
	v_add_f32_e32 v128, v126, v127
	v_lshlrev_b64 v[126:127], 6, v[208:209]
	v_lshl_add_u64 v[126:127], s[22:23], 0, v[126:127]
	global_store_dword v[126:127], v128, off sc1
; __device__ __forceinline__ void st16_wt(void* p, u32x4 v) { asm volatile("global_store_dwordx4 %0, %1, off sc1\n\ts_nop 1" :: "v"(p), "v"(v) : "memory"); }
; __device__ __forceinline__ unsigned cvt_pk_bf16(float lo, float hi) { unsigned r; asm volatile("v_cvt_pk_bf16_f32 %0, %1, %2" : "=v"(r) : "v"(lo), "v"(hi)); return r; }
;     __device__ __forceinline__ void operator()(const Acc& acc, const Unit& u, int wr, int wc, int fr, int fq, const LAS float* tab) const {
;     ...
;                 const size_t row = (size_t)u.pm * BM + ai * HALF + wr * 64 + m * 16 + fr; const size_t off = row * D + col0; float ss = 0.f;
; #pragma unroll
;                 for (int bj = 0; bj < 2; ++bj) { f32x4 b0, b1;
;                     if (base32) { b0 = __builtin_nontemporal_load((const f32x4*)(base32 + off + bj * HALF)); b1 = __builtin_nontemporal_load((const f32x4*)(base32 + off + bj * HALF + 4)); }
;                     else { const u32x4 b4 = rb[ai][m][bj];
;                         b0 = (f32x4){__uint_as_float(b4.x << 16), __uint_as_float(b4.x & 0xFFFF0000u), __uint_as_float(b4.y << 16), __uint_as_float(b4.y & 0xFFFF0000u)};
;                         b1 = (f32x4){__uint_as_float(b4.z << 16), __uint_as_float(b4.z & 0xFFFF0000u), __uint_as_float(b4.w << 16), __uint_as_float(b4.w & 0xFFFF0000u)}; }
;                     const f32x4 o0 = b0 + acc[ai][bj][m][0], o1 = b1 + acc[ai][bj][m][1];
;                     if (out32) {
;                         if (!dry) { *(f32x4*)(out32 + off + bj * HALF) = o0; *(f32x4*)(out32 + off + bj * HALF + 4) = o1; }
;                         continue; }
;                     ss += ((o0[0] * o0[0] + o0[1] * o0[1]) + (o0[2] * o0[2] + o0[3] * o0[3])) + ((o1[0] * o1[0] + o1[1] * o1[1]) + (o1[2] * o1[2] + o1[3] * o1[3]));
;                     u32x4 w; w.x = cvt_pk_bf16(o0[0], o0[1]); w.y = cvt_pk_bf16(o0[2], o0[3]); w.z = cvt_pk_bf16(o1[0], o1[1]); w.w = cvt_pk_bf16(o1[2], o1[3]);
;                     if (!dry) st16_wt(xb + off + bj * HALF, w); }
;                 if (out32) continue;
;                 ss = sum_rows4(ss);
;                 if (fq == 0 && !dry) ssp[row * 16 + u.pn * 4 + wc] = ss;
.LBB0_440:
	s_or_b64 exec, exec, s[24:25]
	v_lshlrev_b32_e32 v130, 16, v182
	v_and_b32_e32 v131, 0xffff0000, v182
	v_lshlrev_b32_e32 v132, 16, v183
	v_and_b32_e32 v133, 0xffff0000, v183
	v_lshlrev_b32_e32 v150, 16, v184
	v_and_b32_e32 v151, 0xffff0000, v184
	v_lshlrev_b32_e32 v152, 16, v185
	v_and_b32_e32 v153, 0xffff0000, v185
	v_pk_add_f32 v[120:121], v[120:121], v[132:133]
	v_pk_add_f32 v[118:119], v[118:119], v[130:131]
	v_pk_add_f32 v[130:131], v[116:117], v[152:153]
	v_pk_add_f32 v[116:117], v[114:115], v[150:151]
	v_mul_f32_e32 v114, v119, v119
	v_mul_f32_e32 v115, v121, v121
	v_fmac_f32_e32 v114, v118, v118
	v_fmac_f32_e32 v115, v120, v120
	v_add_f32_e32 v114, v114, v115
	v_mul_f32_e32 v115, v117, v117
	v_mul_f32_e32 v132, v131, v131
	v_or_b32_e32 v126, 16, v208
	v_mov_b32_e32 v127, v209
	v_fmac_f32_e32 v115, v116, v116
	v_fmac_f32_e32 v132, v130, v130
	v_lshlrev_b64 v[128:129], 11, v[126:127]
	v_add_f32_e32 v115, v115, v132
	v_lshl_add_u64 v[128:129], s[10:11], 0, v[128:129]
	v_add_f32_e32 v132, v114, v115
	v_cvt_pk_bf16_f32 v114, v118, v119
	v_cvt_pk_bf16_f32 v115, v120, v121
	v_cvt_pk_bf16_f32 v116, v116, v117
	v_cvt_pk_bf16_f32 v117, v130, v131
	v_lshl_add_u64 v[128:129], v[206:207], 1, v[128:129]
	global_store_dwordx4 v[128:129], v[114:117], off sc1
	s_nop 1
	v_lshlrev_b32_e32 v114, 16, v178
	v_and_b32_e32 v115, 0xffff0000, v178
	v_lshlrev_b32_e32 v116, 16, v179
	v_and_b32_e32 v117, 0xffff0000, v179
	v_lshlrev_b32_e32 v118, 16, v180
	v_and_b32_e32 v119, 0xffff0000, v180
	v_lshlrev_b32_e32 v120, 16, v181
	v_and_b32_e32 v121, 0xffff0000, v181
	v_pk_add_f32 v[108:109], v[108:109], v[116:117]
	v_pk_add_f32 v[106:107], v[106:107], v[114:115]
	v_pk_add_f32 v[114:115], v[104:105], v[120:121]
	v_pk_add_f32 v[104:105], v[102:103], v[118:119]
	v_mul_f32_e32 v102, v107, v107
	v_mul_f32_e32 v103, v109, v109
	v_fmac_f32_e32 v102, v106, v106
	v_fmac_f32_e32 v103, v108, v108
	v_add_f32_e32 v102, v102, v103
	v_mul_f32_e32 v103, v105, v105
	v_mul_f32_e32 v116, v115, v115
	v_fmac_f32_e32 v103, v104, v104
	v_fmac_f32_e32 v116, v114, v114
	v_add_f32_e32 v103, v103, v116
	v_add_f32_e32 v102, v102, v103
	v_add_f32_e32 v116, v132, v102
	v_cvt_pk_bf16_f32 v102, v106, v107
	v_cvt_pk_bf16_f32 v103, v108, v109
	v_cvt_pk_bf16_f32 v104, v104, v105
	v_cvt_pk_bf16_f32 v105, v114, v115
	v_lshl_add_u64 v[106:107], v[128:129], 0, s[0:1]
	global_store_dwordx4 v[106:107], v[102:105], off sc1
	s_nop 1
	v_mov_b32_e32 v102, v116
	s_nop 1
	v_permlane16_swap_b32_e32 v116, v102
	v_add_f32_e32 v102, v116, v102
	v_mov_b32_e32 v103, v102
	s_nop 1
	v_permlane32_swap_b32_e32 v102, v103
	s_and_saveexec_b64 s[24:25], s[4:5]
	s_cbranch_execz .LBB0_442
	v_add_f32_e32 v104, v102, v103
	v_lshlrev_b64 v[102:103], 6, v[126:127]
	v_lshl_add_u64 v[102:103], s[22:23], 0, v[102:103]
	global_store_dword v[102:103], v104, off sc1
.LBB0_442:
	s_or_b64 exec, exec, s[24:25]
	v_lshlrev_b32_e32 v106, 16, v174
	v_and_b32_e32 v107, 0xffff0000, v174
	v_lshlrev_b32_e32 v108, 16, v175
	v_and_b32_e32 v109, 0xffff0000, v175
	v_lshlrev_b32_e32 v114, 16, v176
	v_and_b32_e32 v115, 0xffff0000, v176
	v_lshlrev_b32_e32 v116, 16, v177
	v_and_b32_e32 v117, 0xffff0000, v177
	v_pk_add_f32 v[96:97], v[96:97], v[108:109]
	v_pk_add_f32 v[94:95], v[94:95], v[106:107]
	v_pk_add_f32 v[106:107], v[92:93], v[116:117]
	v_pk_add_f32 v[92:93], v[90:91], v[114:115]
	v_mul_f32_e32 v90, v95, v95
	v_mul_f32_e32 v91, v97, v97
	v_fmac_f32_e32 v90, v94, v94
	v_fmac_f32_e32 v91, v96, v96
	v_add_f32_e32 v90, v90, v91
	v_mul_f32_e32 v91, v93, v93
	v_mul_f32_e32 v108, v107, v107
	v_or_b32_e32 v102, 32, v208
	v_mov_b32_e32 v103, v209
	v_fmac_f32_e32 v91, v92, v92
	v_fmac_f32_e32 v108, v106, v106
	v_lshlrev_b64 v[104:105], 11, v[102:103]
	v_add_f32_e32 v91, v91, v108
	v_lshl_add_u64 v[104:105], s[10:11], 0, v[104:105]
	v_add_f32_e32 v108, v90, v91
	v_cvt_pk_bf16_f32 v90, v94, v95
	v_cvt_pk_bf16_f32 v91, v96, v97
	v_cvt_pk_bf16_f32 v92, v92, v93
	v_cvt_pk_bf16_f32 v93, v106, v107
	v_lshl_add_u64 v[104:105], v[206:207], 1, v[104:105]
	global_store_dwordx4 v[104:105], v[90:93], off sc1
	s_nop 1
	v_lshlrev_b32_e32 v90, 16, v170
	v_and_b32_e32 v91, 0xffff0000, v170
	v_lshlrev_b32_e32 v92, 16, v171
	v_and_b32_e32 v93, 0xffff0000, v171
	v_lshlrev_b32_e32 v94, 16, v172
	v_and_b32_e32 v95, 0xffff0000, v172
	v_lshlrev_b32_e32 v96, 16, v173
	v_and_b32_e32 v97, 0xffff0000, v173
	v_pk_add_f32 v[88:89], v[88:89], v[92:93]
	v_pk_add_f32 v[86:87], v[86:87], v[90:91]
	v_pk_add_f32 v[90:91], v[84:85], v[96:97]
	v_pk_add_f32 v[84:85], v[82:83], v[94:95]
	v_mul_f32_e32 v82, v87, v87
	v_mul_f32_e32 v83, v89, v89
	v_fmac_f32_e32 v82, v86, v86
	v_fmac_f32_e32 v83, v88, v88
	v_add_f32_e32 v82, v82, v83
	v_mul_f32_e32 v83, v85, v85
	v_mul_f32_e32 v92, v91, v91
	v_fmac_f32_e32 v83, v84, v84
	v_fmac_f32_e32 v92, v90, v90
	v_add_f32_e32 v83, v83, v92
	v_add_f32_e32 v82, v82, v83
	v_add_f32_e32 v92, v108, v82
	v_cvt_pk_bf16_f32 v82, v86, v87
	v_cvt_pk_bf16_f32 v83, v88, v89
	v_cvt_pk_bf16_f32 v84, v84, v85
	v_cvt_pk_bf16_f32 v85, v90, v91
	v_lshl_add_u64 v[86:87], v[104:105], 0, s[0:1]
	global_store_dwordx4 v[86:87], v[82:85], off sc1
	s_nop 1
	v_mov_b32_e32 v82, v92
	s_nop 1
	v_permlane16_swap_b32_e32 v92, v82
	v_add_f32_e32 v82, v92, v82
	v_mov_b32_e32 v83, v82
	s_nop 1
	v_permlane32_swap_b32_e32 v82, v83
	s_and_saveexec_b64 s[24:25], s[4:5]
	s_cbranch_execz .LBB0_444
	v_add_f32_e32 v84, v82, v83
	v_lshlrev_b64 v[82:83], 6, v[102:103]
	v_lshl_add_u64 v[82:83], s[22:23], 0, v[82:83]
	global_store_dword v[82:83], v84, off sc1
; __device__ __forceinline__ void st16_wt(void* p, u32x4 v) { asm volatile("global_store_dwordx4 %0, %1, off sc1\n\ts_nop 1" :: "v"(p), "v"(v) : "memory"); }
; __device__ __forceinline__ unsigned cvt_pk_bf16(float lo, float hi) { unsigned r; asm volatile("v_cvt_pk_bf16_f32 %0, %1, %2" : "=v"(r) : "v"(lo), "v"(hi)); return r; }
;     __device__ __forceinline__ void operator()(const Acc& acc, const Unit& u, int wr, int wc, int fr, int fq, const LAS float* tab) const {
;     ...
;                 const size_t row = (size_t)u.pm * BM + ai * HALF + wr * 64 + m * 16 + fr; const size_t off = row * D + col0; float ss = 0.f;
; #pragma unroll
;                 for (int bj = 0; bj < 2; ++bj) { f32x4 b0, b1;
;                     if (base32) { b0 = __builtin_nontemporal_load((const f32x4*)(base32 + off + bj * HALF)); b1 = __builtin_nontemporal_load((const f32x4*)(base32 + off + bj * HALF + 4)); }
;                     else { const u32x4 b4 = rb[ai][m][bj];
;                         b0 = (f32x4){__uint_as_float(b4.x << 16), __uint_as_float(b4.x & 0xFFFF0000u), __uint_as_float(b4.y << 16), __uint_as_float(b4.y & 0xFFFF0000u)};
;                         b1 = (f32x4){__uint_as_float(b4.z << 16), __uint_as_float(b4.z & 0xFFFF0000u), __uint_as_float(b4.w << 16), __uint_as_float(b4.w & 0xFFFF0000u)}; }
;                     const f32x4 o0 = b0 + acc[ai][bj][m][0], o1 = b1 + acc[ai][bj][m][1];
;                     if (out32) {
;                         if (!dry) { *(f32x4*)(out32 + off + bj * HALF) = o0; *(f32x4*)(out32 + off + bj * HALF + 4) = o1; }
;                         continue; }
;                     ss += ((o0[0] * o0[0] + o0[1] * o0[1]) + (o0[2] * o0[2] + o0[3] * o0[3])) + ((o1[0] * o1[0] + o1[1] * o1[1]) + (o1[2] * o1[2] + o1[3] * o1[3]));
;                     u32x4 w; w.x = cvt_pk_bf16(o0[0], o0[1]); w.y = cvt_pk_bf16(o0[2], o0[3]); w.z = cvt_pk_bf16(o1[0], o1[1]); w.w = cvt_pk_bf16(o1[2], o1[3]);
;                     if (!dry) st16_wt(xb + off + bj * HALF, w); }
;                 if (out32) continue;
;                 ss = sum_rows4(ss);
;                 if (fq == 0 && !dry) ssp[row * 16 + u.pn * 4 + wc] = ss;
.LBB0_444:
	s_or_b64 exec, exec, s[24:25]
	v_lshlrev_b32_e32 v86, 16, v166
	v_and_b32_e32 v87, 0xffff0000, v166
	v_lshlrev_b32_e32 v88, 16, v167
	v_and_b32_e32 v89, 0xffff0000, v167
	v_lshlrev_b32_e32 v90, 16, v168
	v_and_b32_e32 v91, 0xffff0000, v168
	v_lshlrev_b32_e32 v92, 16, v169
	v_and_b32_e32 v93, 0xffff0000, v169
	v_pk_add_f32 v[80:81], v[80:81], v[88:89]
	v_pk_add_f32 v[78:79], v[78:79], v[86:87]
	v_pk_add_f32 v[86:87], v[76:77], v[92:93]
	v_pk_add_f32 v[76:77], v[74:75], v[90:91]
	v_mul_f32_e32 v74, v79, v79
	v_mul_f32_e32 v75, v81, v81
	v_fmac_f32_e32 v74, v78, v78
	v_fmac_f32_e32 v75, v80, v80
	v_add_f32_e32 v74, v74, v75
	v_mul_f32_e32 v75, v77, v77
	v_mul_f32_e32 v88, v87, v87
	v_or_b32_e32 v82, 48, v208
	v_mov_b32_e32 v83, v209
	v_fmac_f32_e32 v75, v76, v76
	v_fmac_f32_e32 v88, v86, v86
	v_lshlrev_b64 v[84:85], 11, v[82:83]
	v_add_f32_e32 v75, v75, v88
	v_lshl_add_u64 v[84:85], s[10:11], 0, v[84:85]
	v_add_f32_e32 v88, v74, v75
	v_cvt_pk_bf16_f32 v74, v78, v79
	v_cvt_pk_bf16_f32 v75, v80, v81
	v_cvt_pk_bf16_f32 v76, v76, v77
	v_cvt_pk_bf16_f32 v77, v86, v87
	v_lshl_add_u64 v[84:85], v[206:207], 1, v[84:85]
	global_store_dwordx4 v[84:85], v[74:77], off sc1
	s_nop 1
	v_lshlrev_b32_e32 v74, 16, v162
	v_and_b32_e32 v75, 0xffff0000, v162
	v_lshlrev_b32_e32 v76, 16, v163
	v_and_b32_e32 v77, 0xffff0000, v163
	v_lshlrev_b32_e32 v78, 16, v164
	v_and_b32_e32 v79, 0xffff0000, v164
	v_lshlrev_b32_e32 v80, 16, v165
	v_and_b32_e32 v81, 0xffff0000, v165
	v_pk_add_f32 v[72:73], v[72:73], v[76:77]
	v_pk_add_f32 v[70:71], v[70:71], v[74:75]
	v_pk_add_f32 v[74:75], v[68:69], v[80:81]
	v_pk_add_f32 v[68:69], v[66:67], v[78:79]
	v_mul_f32_e32 v66, v71, v71
	v_mul_f32_e32 v67, v73, v73
	v_fmac_f32_e32 v66, v70, v70
	v_fmac_f32_e32 v67, v72, v72
	v_add_f32_e32 v66, v66, v67
	v_mul_f32_e32 v67, v69, v69
	v_mul_f32_e32 v76, v75, v75
	v_fmac_f32_e32 v67, v68, v68
	v_fmac_f32_e32 v76, v74, v74
	v_add_f32_e32 v67, v67, v76
	v_add_f32_e32 v66, v66, v67
	v_add_f32_e32 v76, v88, v66
	v_cvt_pk_bf16_f32 v66, v70, v71
	v_cvt_pk_bf16_f32 v67, v72, v73
	v_cvt_pk_bf16_f32 v68, v68, v69
	v_cvt_pk_bf16_f32 v69, v74, v75
	v_lshl_add_u64 v[70:71], v[84:85], 0, s[0:1]
	global_store_dwordx4 v[70:71], v[66:69], off sc1
	s_nop 1
	v_mov_b32_e32 v66, v76
	s_nop 1
	v_permlane16_swap_b32_e32 v76, v66
	v_add_f32_e32 v66, v76, v66
	v_mov_b32_e32 v67, v66
	s_nop 1
	v_permlane32_swap_b32_e32 v66, v67
	s_and_saveexec_b64 s[24:25], s[4:5]
	s_cbranch_execz .LBB0_446
	v_add_f32_e32 v68, v66, v67
	v_lshlrev_b64 v[66:67], 6, v[82:83]
	v_lshl_add_u64 v[66:67], s[22:23], 0, v[66:67]
	global_store_dword v[66:67], v68, off sc1
.LBB0_446:
	s_or_b64 exec, exec, s[24:25]
	v_lshlrev_b32_e32 v70, 16, v158
	v_and_b32_e32 v71, 0xffff0000, v158
	v_lshlrev_b32_e32 v72, 16, v159
	v_and_b32_e32 v73, 0xffff0000, v159
	v_lshlrev_b32_e32 v74, 16, v160
	v_and_b32_e32 v75, 0xffff0000, v160
	v_lshlrev_b32_e32 v76, 16, v161
	v_and_b32_e32 v77, 0xffff0000, v161
	v_pk_add_f32 v[64:65], v[64:65], v[72:73]
	v_pk_add_f32 v[62:63], v[62:63], v[70:71]
	v_pk_add_f32 v[70:71], v[60:61], v[76:77]
	v_pk_add_f32 v[60:61], v[58:59], v[74:75]
	v_mul_f32_e32 v58, v63, v63
	v_mul_f32_e32 v59, v65, v65
	v_fmac_f32_e32 v58, v62, v62
	v_fmac_f32_e32 v59, v64, v64
	v_add_f32_e32 v58, v58, v59
	v_mul_f32_e32 v59, v61, v61
	v_mul_f32_e32 v72, v71, v71
	v_lshl_add_u64 v[66:67], v[208:209], 0, s[90:91]
	v_fmac_f32_e32 v59, v60, v60
	v_fmac_f32_e32 v72, v70, v70
	v_lshlrev_b64 v[68:69], 11, v[66:67]
	v_add_f32_e32 v59, v59, v72
	v_lshl_add_u64 v[68:69], s[10:11], 0, v[68:69]
	v_add_f32_e32 v72, v58, v59
	v_cvt_pk_bf16_f32 v58, v62, v63
	v_cvt_pk_bf16_f32 v59, v64, v65
	v_cvt_pk_bf16_f32 v60, v60, v61
	v_cvt_pk_bf16_f32 v61, v70, v71
	v_lshl_add_u64 v[68:69], v[206:207], 1, v[68:69]
	global_store_dwordx4 v[68:69], v[58:61], off sc1
	s_nop 1
	v_lshlrev_b32_e32 v58, 16, v146
	v_and_b32_e32 v59, 0xffff0000, v146
	v_lshlrev_b32_e32 v60, 16, v147
	v_and_b32_e32 v61, 0xffff0000, v147
	v_lshlrev_b32_e32 v62, 16, v148
	v_and_b32_e32 v63, 0xffff0000, v148
	v_lshlrev_b32_e32 v64, 16, v149
	v_and_b32_e32 v65, 0xffff0000, v149
	v_pk_add_f32 v[56:57], v[56:57], v[60:61]
	v_pk_add_f32 v[54:55], v[54:55], v[58:59]
	v_pk_add_f32 v[58:59], v[52:53], v[64:65]
	v_pk_add_f32 v[52:53], v[50:51], v[62:63]
	v_mul_f32_e32 v50, v55, v55
	v_mul_f32_e32 v51, v57, v57
	v_fmac_f32_e32 v50, v54, v54
	v_fmac_f32_e32 v51, v56, v56
	v_add_f32_e32 v50, v50, v51
	v_mul_f32_e32 v51, v53, v53
	v_mul_f32_e32 v60, v59, v59
	v_fmac_f32_e32 v51, v52, v52
	v_fmac_f32_e32 v60, v58, v58
	v_add_f32_e32 v51, v51, v60
	v_add_f32_e32 v50, v50, v51
	v_add_f32_e32 v60, v72, v50
	v_cvt_pk_bf16_f32 v50, v54, v55
	v_cvt_pk_bf16_f32 v51, v56, v57
	v_cvt_pk_bf16_f32 v52, v52, v53
	v_cvt_pk_bf16_f32 v53, v58, v59
	v_lshl_add_u64 v[54:55], v[68:69], 0, s[0:1]
	global_store_dwordx4 v[54:55], v[50:53], off sc1
	s_nop 1
	v_mov_b32_e32 v50, v60
	s_nop 1
	v_permlane16_swap_b32_e32 v60, v50
	v_add_f32_e32 v50, v60, v50
	v_mov_b32_e32 v51, v50
	s_nop 1
	v_permlane32_swap_b32_e32 v50, v51
	s_and_saveexec_b64 s[24:25], s[4:5]
	s_cbranch_execz .LBB0_448
	v_add_f32_e32 v52, v50, v51
	v_lshlrev_b64 v[50:51], 6, v[66:67]
	v_lshl_add_u64 v[50:51], s[22:23], 0, v[50:51]
	global_store_dword v[50:51], v52, off sc1
; __device__ __forceinline__ void st16_wt(void* p, u32x4 v) { asm volatile("global_store_dwordx4 %0, %1, off sc1\n\ts_nop 1" :: "v"(p), "v"(v) : "memory"); }
; __device__ __forceinline__ unsigned cvt_pk_bf16(float lo, float hi) { unsigned r; asm volatile("v_cvt_pk_bf16_f32 %0, %1, %2" : "=v"(r) : "v"(lo), "v"(hi)); return r; }
;     __device__ __forceinline__ void operator()(const Acc& acc, const Unit& u, int wr, int wc, int fr, int fq, const LAS float* tab) const {
;     ...
;                 const size_t row = (size_t)u.pm * BM + ai * HALF + wr * 64 + m * 16 + fr; const size_t off = row * D + col0; float ss = 0.f;
; #pragma unroll
;                 for (int bj = 0; bj < 2; ++bj) { f32x4 b0, b1;
;                     if (base32) { b0 = __builtin_nontemporal_load((const f32x4*)(base32 + off + bj * HALF)); b1 = __builtin_nontemporal_load((const f32x4*)(base32 + off + bj * HALF + 4)); }
;                     else { const u32x4 b4 = rb[ai][m][bj];
;                         b0 = (f32x4){__uint_as_float(b4.x << 16), __uint_as_float(b4.x & 0xFFFF0000u), __uint_as_float(b4.y << 16), __uint_as_float(b4.y & 0xFFFF0000u)};
;                         b1 = (f32x4){__uint_as_float(b4.z << 16), __uint_as_float(b4.z & 0xFFFF0000u), __uint_as_float(b4.w << 16), __uint_as_float(b4.w & 0xFFFF0000u)}; }
;                     const f32x4 o0 = b0 + acc[ai][bj][m][0], o1 = b1 + acc[ai][bj][m][1];
;                     if (out32) {
;                         if (!dry) { *(f32x4*)(out32 + off + bj * HALF) = o0; *(f32x4*)(out32 + off + bj * HALF + 4) = o1; }
;                         continue; }
;                     ss += ((o0[0] * o0[0] + o0[1] * o0[1]) + (o0[2] * o0[2] + o0[3] * o0[3])) + ((o1[0] * o1[0] + o1[1] * o1[1]) + (o1[2] * o1[2] + o1[3] * o1[3]));
;                     u32x4 w; w.x = cvt_pk_bf16(o0[0], o0[1]); w.y = cvt_pk_bf16(o0[2], o0[3]); w.z = cvt_pk_bf16(o1[0], o1[1]); w.w = cvt_pk_bf16(o1[2], o1[3]);
;                     if (!dry) st16_wt(xb + off + bj * HALF, w); }
;                 if (out32) continue;
;                 ss = sum_rows4(ss);
;                 if (fq == 0 && !dry) ssp[row * 16 + u.pn * 4 + wc] = ss;
.LBB0_448:
	s_or_b64 exec, exec, s[24:25]
	v_lshlrev_b32_e32 v54, 16, v142
	v_and_b32_e32 v55, 0xffff0000, v142
	v_lshlrev_b32_e32 v56, 16, v143
	v_and_b32_e32 v57, 0xffff0000, v143
	v_lshlrev_b32_e32 v58, 16, v144
	v_and_b32_e32 v59, 0xffff0000, v144
	v_lshlrev_b32_e32 v60, 16, v145
	v_and_b32_e32 v61, 0xffff0000, v145
	v_pk_add_f32 v[48:49], v[48:49], v[56:57]
	v_pk_add_f32 v[46:47], v[46:47], v[54:55]
	v_pk_add_f32 v[54:55], v[44:45], v[60:61]
	v_pk_add_f32 v[44:45], v[42:43], v[58:59]
	v_mul_f32_e32 v42, v47, v47
	v_mul_f32_e32 v43, v49, v49
	v_fmac_f32_e32 v42, v46, v46
	v_fmac_f32_e32 v43, v48, v48
	s_mov_b64 s[0:1], 0x90
	v_add_f32_e32 v42, v42, v43
	v_mul_f32_e32 v43, v45, v45
	v_mul_f32_e32 v56, v55, v55
	v_lshl_add_u64 v[50:51], v[208:209], 0, s[0:1]
	v_fmac_f32_e32 v43, v44, v44
	v_fmac_f32_e32 v56, v54, v54
	v_lshlrev_b64 v[52:53], 11, v[50:51]
	v_add_f32_e32 v43, v43, v56
	v_lshl_add_u64 v[52:53], s[10:11], 0, v[52:53]
	v_add_f32_e32 v56, v42, v43
	v_cvt_pk_bf16_f32 v42, v46, v47
	v_cvt_pk_bf16_f32 v43, v48, v49
	v_cvt_pk_bf16_f32 v44, v44, v45
	v_cvt_pk_bf16_f32 v45, v54, v55
	v_lshl_add_u64 v[52:53], v[206:207], 1, v[52:53]
	global_store_dwordx4 v[52:53], v[42:45], off sc1
	s_nop 1
	v_lshlrev_b32_e32 v42, 16, v138
	v_and_b32_e32 v43, 0xffff0000, v138
	v_lshlrev_b32_e32 v44, 16, v139
	v_and_b32_e32 v45, 0xffff0000, v139
	v_lshlrev_b32_e32 v46, 16, v140
	v_and_b32_e32 v47, 0xffff0000, v140
	v_lshlrev_b32_e32 v48, 16, v141
	v_and_b32_e32 v49, 0xffff0000, v141
	v_pk_add_f32 v[40:41], v[40:41], v[44:45]
	v_pk_add_f32 v[38:39], v[38:39], v[42:43]
	v_pk_add_f32 v[42:43], v[36:37], v[48:49]
	v_pk_add_f32 v[36:37], v[34:35], v[46:47]
	v_mul_f32_e32 v34, v39, v39
	v_mul_f32_e32 v35, v41, v41
	v_fmac_f32_e32 v34, v38, v38
	v_fmac_f32_e32 v35, v40, v40
	v_add_f32_e32 v34, v34, v35
	v_mul_f32_e32 v35, v37, v37
	v_mul_f32_e32 v44, v43, v43
	v_fmac_f32_e32 v35, v36, v36
	v_fmac_f32_e32 v44, v42, v42
	v_add_f32_e32 v35, v35, v44
	v_add_f32_e32 v34, v34, v35
	v_add_f32_e32 v44, v56, v34
	v_cvt_pk_bf16_f32 v34, v38, v39
	s_mov_b64 s[0:1], 0x100
	v_cvt_pk_bf16_f32 v35, v40, v41
	v_cvt_pk_bf16_f32 v36, v36, v37
	v_cvt_pk_bf16_f32 v37, v42, v43
	v_lshl_add_u64 v[38:39], v[52:53], 0, s[0:1]
	global_store_dwordx4 v[38:39], v[34:37], off sc1
	s_nop 1
	v_mov_b32_e32 v34, v44
	s_nop 1
	v_permlane16_swap_b32_e32 v44, v34
	v_add_f32_e32 v34, v44, v34
	v_mov_b32_e32 v35, v34
	s_nop 1
	v_permlane32_swap_b32_e32 v34, v35
	s_and_saveexec_b64 s[24:25], s[4:5]
	s_cbranch_execz .LBB0_450
	v_add_f32_e32 v36, v34, v35
	v_lshlrev_b64 v[34:35], 6, v[50:51]
	v_lshl_add_u64 v[34:35], s[22:23], 0, v[34:35]
	global_store_dword v[34:35], v36, off sc1
; __device__ __forceinline__ void st16_wt(void* p, u32x4 v) { asm volatile("global_store_dwordx4 %0, %1, off sc1\n\ts_nop 1" :: "v"(p), "v"(v) : "memory"); }
; __device__ __forceinline__ unsigned cvt_pk_bf16(float lo, float hi) { unsigned r; asm volatile("v_cvt_pk_bf16_f32 %0, %1, %2" : "=v"(r) : "v"(lo), "v"(hi)); return r; }
;     __device__ __forceinline__ void operator()(const Acc& acc, const Unit& u, int wr, int wc, int fr, int fq, const LAS float* tab) const {
;     ...
;                 const size_t row = (size_t)u.pm * BM + ai * HALF + wr * 64 + m * 16 + fr; const size_t off = row * D + col0; float ss = 0.f;
; #pragma unroll
;                 for (int bj = 0; bj < 2; ++bj) { f32x4 b0, b1;
;                     if (base32) { b0 = __builtin_nontemporal_load((const f32x4*)(base32 + off + bj * HALF)); b1 = __builtin_nontemporal_load((const f32x4*)(base32 + off + bj * HALF + 4)); }
;                     else { const u32x4 b4 = rb[ai][m][bj];
;                         b0 = (f32x4){__uint_as_float(b4.x << 16), __uint_as_float(b4.x & 0xFFFF0000u), __uint_as_float(b4.y << 16), __uint_as_float(b4.y & 0xFFFF0000u)};
;                         b1 = (f32x4){__uint_as_float(b4.z << 16), __uint_as_float(b4.z & 0xFFFF0000u), __uint_as_float(b4.w << 16), __uint_as_float(b4.w & 0xFFFF0000u)}; }
;                     const f32x4 o0 = b0 + acc[ai][bj][m][0], o1 = b1 + acc[ai][bj][m][1];
;                     if (out32) {
;                         if (!dry) { *(f32x4*)(out32 + off + bj * HALF) = o0; *(f32x4*)(out32 + off + bj * HALF + 4) = o1; }
;                         continue; }
;                     ss += ((o0[0] * o0[0] + o0[1] * o0[1]) + (o0[2] * o0[2] + o0[3] * o0[3])) + ((o1[0] * o1[0] + o1[1] * o1[1]) + (o1[2] * o1[2] + o1[3] * o1[3]));
;                     u32x4 w; w.x = cvt_pk_bf16(o0[0], o0[1]); w.y = cvt_pk_bf16(o0[2], o0[3]); w.z = cvt_pk_bf16(o1[0], o1[1]); w.w = cvt_pk_bf16(o1[2], o1[3]);
;                     if (!dry) st16_wt(xb + off + bj * HALF, w); }
;                 if (out32) continue;
;                 ss = sum_rows4(ss);
;                 if (fq == 0 && !dry) ssp[row * 16 + u.pn * 4 + wc] = ss;
.LBB0_450:
	s_or_b64 exec, exec, s[24:25]
	v_lshlrev_b32_e32 v38, 16, v134
	v_and_b32_e32 v39, 0xffff0000, v134
	v_lshlrev_b32_e32 v40, 16, v135
	v_and_b32_e32 v41, 0xffff0000, v135
	v_lshlrev_b32_e32 v42, 16, v136
	v_and_b32_e32 v43, 0xffff0000, v136
	v_lshlrev_b32_e32 v44, 16, v137
	v_and_b32_e32 v45, 0xffff0000, v137
	v_pk_add_f32 v[32:33], v[32:33], v[40:41]
	v_pk_add_f32 v[30:31], v[30:31], v[38:39]
	v_pk_add_f32 v[38:39], v[28:29], v[44:45]
	v_pk_add_f32 v[28:29], v[26:27], v[42:43]
	v_mul_f32_e32 v26, v31, v31
	v_mul_f32_e32 v27, v33, v33
	v_fmac_f32_e32 v26, v30, v30
	v_fmac_f32_e32 v27, v32, v32
	s_mov_b64 s[0:1], 0xa0
	v_add_f32_e32 v26, v26, v27
	v_mul_f32_e32 v27, v29, v29
	v_mul_f32_e32 v40, v39, v39
	v_lshl_add_u64 v[34:35], v[208:209], 0, s[0:1]
	v_fmac_f32_e32 v27, v28, v28
	v_fmac_f32_e32 v40, v38, v38
	v_lshlrev_b64 v[36:37], 11, v[34:35]
	v_add_f32_e32 v27, v27, v40
	v_lshl_add_u64 v[36:37], s[10:11], 0, v[36:37]
	v_add_f32_e32 v40, v26, v27
	v_cvt_pk_bf16_f32 v26, v30, v31
	v_cvt_pk_bf16_f32 v27, v32, v33
	v_cvt_pk_bf16_f32 v28, v28, v29
	v_cvt_pk_bf16_f32 v29, v38, v39
	v_lshl_add_u64 v[36:37], v[206:207], 1, v[36:37]
	global_store_dwordx4 v[36:37], v[26:29], off sc1
	s_nop 1
	v_lshlrev_b32_e32 v26, 16, v122
	v_and_b32_e32 v27, 0xffff0000, v122
	v_lshlrev_b32_e32 v28, 16, v123
	v_and_b32_e32 v29, 0xffff0000, v123
	v_lshlrev_b32_e32 v30, 16, v124
	v_and_b32_e32 v31, 0xffff0000, v124
	v_lshlrev_b32_e32 v32, 16, v125
	v_and_b32_e32 v33, 0xffff0000, v125
	v_pk_add_f32 v[24:25], v[24:25], v[28:29]
	v_pk_add_f32 v[22:23], v[22:23], v[26:27]
	v_pk_add_f32 v[26:27], v[20:21], v[32:33]
	v_pk_add_f32 v[20:21], v[18:19], v[30:31]
	v_mul_f32_e32 v18, v23, v23
	v_mul_f32_e32 v19, v25, v25
	v_fmac_f32_e32 v18, v22, v22
	v_fmac_f32_e32 v19, v24, v24
	v_add_f32_e32 v18, v18, v19
	v_mul_f32_e32 v19, v21, v21
	v_mul_f32_e32 v28, v27, v27
	v_fmac_f32_e32 v19, v20, v20
	v_fmac_f32_e32 v28, v26, v26
	v_add_f32_e32 v19, v19, v28
	v_add_f32_e32 v18, v18, v19
	v_add_f32_e32 v28, v40, v18
	v_cvt_pk_bf16_f32 v18, v22, v23
	s_mov_b64 s[0:1], 0x100
	v_cvt_pk_bf16_f32 v19, v24, v25
	v_cvt_pk_bf16_f32 v20, v20, v21
	v_cvt_pk_bf16_f32 v21, v26, v27
	v_lshl_add_u64 v[22:23], v[36:37], 0, s[0:1]
	global_store_dwordx4 v[22:23], v[18:21], off sc1
	s_nop 1
	v_mov_b32_e32 v18, v28
	s_nop 1
	v_permlane16_swap_b32_e32 v28, v18
	v_add_f32_e32 v18, v28, v18
	v_mov_b32_e32 v19, v18
	s_nop 1
	v_permlane32_swap_b32_e32 v18, v19
	s_and_saveexec_b64 s[24:25], s[4:5]
	s_cbranch_execz .LBB0_452
	v_add_f32_e32 v20, v18, v19
	v_lshlrev_b64 v[18:19], 6, v[34:35]
	v_lshl_add_u64 v[18:19], s[22:23], 0, v[18:19]
	global_store_dword v[18:19], v20, off sc1
.LBB0_452:
	s_or_b64 exec, exec, s[24:25]
	v_lshlrev_b32_e32 v22, 16, v110
	v_and_b32_e32 v23, 0xffff0000, v110
	v_lshlrev_b32_e32 v24, 16, v111
	v_and_b32_e32 v25, 0xffff0000, v111
	v_lshlrev_b32_e32 v26, 16, v112
	v_and_b32_e32 v27, 0xffff0000, v112
	v_lshlrev_b32_e32 v28, 16, v113
	v_and_b32_e32 v29, 0xffff0000, v113
	v_pk_add_f32 v[16:17], v[16:17], v[24:25]
	v_pk_add_f32 v[14:15], v[14:15], v[22:23]
	v_pk_add_f32 v[22:23], v[12:13], v[28:29]
	v_pk_add_f32 v[12:13], v[10:11], v[26:27]
	v_mul_f32_e32 v10, v15, v15
	v_mul_f32_e32 v11, v17, v17
	v_fmac_f32_e32 v10, v14, v14
	v_fmac_f32_e32 v11, v16, v16
	s_mov_b64 s[0:1], 0xb0
	v_add_f32_e32 v10, v10, v11
	v_mul_f32_e32 v11, v13, v13
	v_mul_f32_e32 v24, v23, v23
	v_lshl_add_u64 v[18:19], v[208:209], 0, s[0:1]
	v_fmac_f32_e32 v11, v12, v12
	v_fmac_f32_e32 v24, v22, v22
	v_lshlrev_b64 v[20:21], 11, v[18:19]
	v_add_f32_e32 v11, v11, v24
	v_lshl_add_u64 v[20:21], s[10:11], 0, v[20:21]
	v_add_f32_e32 v24, v10, v11
	v_cvt_pk_bf16_f32 v10, v14, v15
	v_cvt_pk_bf16_f32 v11, v16, v17
	v_cvt_pk_bf16_f32 v12, v12, v13
	v_cvt_pk_bf16_f32 v13, v22, v23
	v_lshl_add_u64 v[20:21], v[206:207], 1, v[20:21]
	global_store_dwordx4 v[20:21], v[10:13], off sc1
	s_nop 1
	v_lshlrev_b32_e32 v10, 16, v98
	v_and_b32_e32 v11, 0xffff0000, v98
	v_lshlrev_b32_e32 v12, 16, v99
	v_and_b32_e32 v13, 0xffff0000, v99
	v_lshlrev_b32_e32 v14, 16, v100
	v_and_b32_e32 v15, 0xffff0000, v100
	v_lshlrev_b32_e32 v16, 16, v101
	v_and_b32_e32 v17, 0xffff0000, v101
	v_pk_add_f32 v[8:9], v[8:9], v[12:13]
	v_pk_add_f32 v[6:7], v[6:7], v[10:11]
	v_pk_add_f32 v[10:11], v[4:5], v[16:17]
	v_pk_add_f32 v[4:5], v[2:3], v[14:15]
	v_mul_f32_e32 v2, v7, v7
	v_mul_f32_e32 v3, v9, v9
	v_fmac_f32_e32 v2, v6, v6
	v_fmac_f32_e32 v3, v8, v8
	v_add_f32_e32 v2, v2, v3
	v_mul_f32_e32 v3, v5, v5
	v_mul_f32_e32 v12, v11, v11
	v_fmac_f32_e32 v3, v4, v4
	v_fmac_f32_e32 v12, v10, v10
	v_add_f32_e32 v3, v3, v12
	v_add_f32_e32 v2, v2, v3
	v_add_f32_e32 v12, v24, v2
	v_cvt_pk_bf16_f32 v2, v6, v7
	s_mov_b64 s[0:1], 0x100
	v_cvt_pk_bf16_f32 v3, v8, v9
	v_cvt_pk_bf16_f32 v4, v4, v5
	v_cvt_pk_bf16_f32 v5, v10, v11
	v_lshl_add_u64 v[6:7], v[20:21], 0, s[0:1]
	global_store_dwordx4 v[6:7], v[2:5], off sc1
	s_nop 1
	v_mov_b32_e32 v2, v12
	s_nop 1
	v_permlane16_swap_b32_e32 v12, v2
	v_add_f32_e32 v2, v12, v2
	v_mov_b32_e32 v3, v2
	s_nop 1
	v_permlane32_swap_b32_e32 v2, v3
	s_and_saveexec_b64 s[24:25], s[4:5]
	s_cbranch_execz .LBB0_454
	v_add_f32_e32 v4, v2, v3
	v_lshlrev_b64 v[2:3], 6, v[18:19]
	v_lshl_add_u64 v[2:3], s[22:23], 0, v[2:3]
	global_store_dword v[2:3], v4, off sc1

;     __device__ __forceinline__ void operator()(const Acc& acc, const Unit& u, int wr, int wc, int fr, int fq, const LAS float* tab) const {
;     ...
;                 const int rl = ai * HALF + wr * 64 + m * 16 + fr; const size_t row = (size_t)u.pm * BM + rl; const float rs = rsv[ai][m];
;                 f32x4 v[2][2]; float ss = 0.f;
; #pragma unroll
;                 for (int bj = 0; bj < 2; ++bj)
; #pragma unroll
;                     for (int n = 0; n < 2; ++n) { v[bj][n] = acc[ai][bj][m][n] * rs; const f32x4 x = v[bj][n]; ss += (x[0] * x[0] + x[1] * x[1]) + (x[2] * x[2] + x[3] * x[3]); }
;                 if (mode == 3) { if (fq == 0) *(f32x4*)(WI + row * 4) = v[0][0]; continue; }
.LBB0_575:
	s_and_b64 vcc, exec, s[12:13]
	s_cbranch_vccz .LBB0_579
	s_and_saveexec_b64 s[12:13], s[6:7]
	s_cbranch_execz .LBB0_578
	v_lshl_add_u64 v[130:131], v[188:189], 4, s[24:25]
	global_store_dwordx4 v[130:131], v[142:145], off sc1

;     __device__ __forceinline__ void operator()(const Acc& acc, const Unit& u, int wr, int wc, int fr, int fq, const LAS float* tab) const {
;     ...
;                 const int rl = ai * HALF + wr * 64 + m * 16 + fr; const size_t row = (size_t)u.pm * BM + rl; const float rs = rsv[ai][m];
;                 f32x4 v[2][2]; float ss = 0.f;
; #pragma unroll
;                 for (int bj = 0; bj < 2; ++bj)
; #pragma unroll
;                     for (int n = 0; n < 2; ++n) { v[bj][n] = acc[ai][bj][m][n] * rs; const f32x4 x = v[bj][n]; ss += (x[0] * x[0] + x[1] * x[1]) + (x[2] * x[2] + x[3] * x[3]); }
;                 if (mode == 3) { if (fq == 0) *(f32x4*)(WI + row * 4) = v[0][0]; continue; }
.LBB0_583:
	s_and_b64 vcc, exec, s[48:49]
	s_cbranch_vccz .LBB0_587
	s_and_saveexec_b64 s[48:49], s[6:7]
	s_cbranch_execz .LBB0_586
	v_lshl_add_u64 v[114:115], v[130:131], 4, s[24:25]
	global_store_dwordx4 v[114:115], v[126:129], off sc1

;     __device__ __forceinline__ void operator()(const Acc& acc, const Unit& u, int wr, int wc, int fr, int fq, const LAS float* tab) const {
;     ...
;                 const int rl = ai * HALF + wr * 64 + m * 16 + fr; const size_t row = (size_t)u.pm * BM + rl; const float rs = rsv[ai][m];
;                 f32x4 v[2][2]; float ss = 0.f;
; #pragma unroll
;                 for (int bj = 0; bj < 2; ++bj)
; #pragma unroll
;                     for (int n = 0; n < 2; ++n) { v[bj][n] = acc[ai][bj][m][n] * rs; const f32x4 x = v[bj][n]; ss += (x[0] * x[0] + x[1] * x[1]) + (x[2] * x[2] + x[3] * x[3]); }
;                 if (mode == 3) { if (fq == 0) *(f32x4*)(WI + row * 4) = v[0][0]; continue; }
.LBB0_591:
	s_and_b64 vcc, exec, s[48:49]
	s_cbranch_vccz .LBB0_595
	s_and_saveexec_b64 s[48:49], s[6:7]
	s_cbranch_execz .LBB0_594
	v_lshl_add_u64 v[86:87], v[114:115], 4, s[24:25]
	global_store_dwordx4 v[86:87], v[106:109], off sc1

;     __device__ __forceinline__ void operator()(const Acc& acc, const Unit& u, int wr, int wc, int fr, int fq, const LAS float* tab) const {
;     ...
;                 const int rl = ai * HALF + wr * 64 + m * 16 + fr; const size_t row = (size_t)u.pm * BM + rl; const float rs = rsv[ai][m];
;                 f32x4 v[2][2]; float ss = 0.f;
; #pragma unroll
;                 for (int bj = 0; bj < 2; ++bj)
; #pragma unroll
;                     for (int n = 0; n < 2; ++n) { v[bj][n] = acc[ai][bj][m][n] * rs; const f32x4 x = v[bj][n]; ss += (x[0] * x[0] + x[1] * x[1]) + (x[2] * x[2] + x[3] * x[3]); }
;                 if (mode == 3) { if (fq == 0) *(f32x4*)(WI + row * 4) = v[0][0]; continue; }
.LBB0_599:
	s_and_b64 vcc, exec, s[48:49]
	s_cbranch_vccz .LBB0_603
	s_and_saveexec_b64 s[48:49], s[6:7]
	s_cbranch_execz .LBB0_602
	v_lshl_add_u64 v[66:67], v[86:87], 4, s[24:25]
	global_store_dwordx4 v[66:67], v[78:81], off sc1

;     __device__ __forceinline__ void operator()(const Acc& acc, const Unit& u, int wr, int wc, int fr, int fq, const LAS float* tab) const {
;     ...
;                 const int rl = ai * HALF + wr * 64 + m * 16 + fr; const size_t row = (size_t)u.pm * BM + rl; const float rs = rsv[ai][m];
;                 f32x4 v[2][2]; float ss = 0.f;
; #pragma unroll
;                 for (int bj = 0; bj < 2; ++bj)
; #pragma unroll
;                     for (int n = 0; n < 2; ++n) { v[bj][n] = acc[ai][bj][m][n] * rs; const f32x4 x = v[bj][n]; ss += (x[0] * x[0] + x[1] * x[1]) + (x[2] * x[2] + x[3] * x[3]); }
;                 if (mode == 3) { if (fq == 0) *(f32x4*)(WI + row * 4) = v[0][0]; continue; }
.LBB0_607:
	s_and_b64 vcc, exec, s[48:49]
	s_cbranch_vccz .LBB0_611
	s_and_saveexec_b64 s[48:49], s[6:7]
	s_cbranch_execz .LBB0_610
	v_lshl_add_u64 v[50:51], v[66:67], 4, s[24:25]
	global_store_dwordx4 v[50:51], v[62:65], off sc1

;     __device__ __forceinline__ void operator()(const Acc& acc, const Unit& u, int wr, int wc, int fr, int fq, const LAS float* tab) const {
;     ...
;                 const int rl = ai * HALF + wr * 64 + m * 16 + fr; const size_t row = (size_t)u.pm * BM + rl; const float rs = rsv[ai][m];
;                 f32x4 v[2][2]; float ss = 0.f;
; #pragma unroll
;                 for (int bj = 0; bj < 2; ++bj)
; #pragma unroll
;                     for (int n = 0; n < 2; ++n) { v[bj][n] = acc[ai][bj][m][n] * rs; const f32x4 x = v[bj][n]; ss += (x[0] * x[0] + x[1] * x[1]) + (x[2] * x[2] + x[3] * x[3]); }
;                 if (mode == 3) { if (fq == 0) *(f32x4*)(WI + row * 4) = v[0][0]; continue; }
.LBB0_615:
	s_and_b64 vcc, exec, s[48:49]
	s_cbranch_vccz .LBB0_619
	s_and_saveexec_b64 s[48:49], s[6:7]
	s_cbranch_execz .LBB0_618
	v_lshl_add_u64 v[34:35], v[50:51], 4, s[24:25]
	global_store_dwordx4 v[34:35], v[46:49], off sc1

;     __device__ __forceinline__ void operator()(const Acc& acc, const Unit& u, int wr, int wc, int fr, int fq, const LAS float* tab) const {
;     ...
;                 const int rl = ai * HALF + wr * 64 + m * 16 + fr; const size_t row = (size_t)u.pm * BM + rl; const float rs = rsv[ai][m];
;                 f32x4 v[2][2]; float ss = 0.f;
; #pragma unroll
;                 for (int bj = 0; bj < 2; ++bj)
; #pragma unroll
;                     for (int n = 0; n < 2; ++n) { v[bj][n] = acc[ai][bj][m][n] * rs; const f32x4 x = v[bj][n]; ss += (x[0] * x[0] + x[1] * x[1]) + (x[2] * x[2] + x[3] * x[3]); }
;                 if (mode == 3) { if (fq == 0) *(f32x4*)(WI + row * 4) = v[0][0]; continue; }
.LBB0_623:
	s_and_b64 vcc, exec, s[48:49]
	s_cbranch_vccz .LBB0_627
	s_and_saveexec_b64 s[48:49], s[6:7]
	s_cbranch_execz .LBB0_626
	v_lshl_add_u64 v[18:19], v[34:35], 4, s[24:25]
	global_store_dwordx4 v[18:19], v[30:33], off sc1

;     __device__ __forceinline__ void operator()(const Acc& acc, const Unit& u, int wr, int wc, int fr, int fq, const LAS float* tab) const {
;     ...
;                 const int rl = ai * HALF + wr * 64 + m * 16 + fr; const size_t row = (size_t)u.pm * BM + rl; const float rs = rsv[ai][m];
;                 f32x4 v[2][2]; float ss = 0.f;
; #pragma unroll
;                 for (int bj = 0; bj < 2; ++bj)
; #pragma unroll
;                     for (int n = 0; n < 2; ++n) { v[bj][n] = acc[ai][bj][m][n] * rs; const f32x4 x = v[bj][n]; ss += (x[0] * x[0] + x[1] * x[1]) + (x[2] * x[2] + x[3] * x[3]); }
;                 if (mode == 3) { if (fq == 0) *(f32x4*)(WI + row * 4) = v[0][0]; continue; }
.LBB0_631:
	s_and_b64 vcc, exec, s[12:13]
	s_cbranch_vccz .LBB0_635
	s_and_saveexec_b64 s[10:11], s[6:7]
	s_cbranch_execz .LBB0_634
	v_lshl_add_u64 v[2:3], v[18:19], 4, s[24:25]
	global_store_dwordx4 v[2:3], v[14:17], off sc1

; __device__ __forceinline__ unsigned xb_ld(unsigned* p)              { return __hip_atomic_load(p, __ATOMIC_RELAXED, __HIP_MEMORY_SCOPE_AGENT); }
; __device__ __forceinline__ unsigned xb_add(unsigned* p, unsigned v) { return __hip_atomic_fetch_add(p, v, __ATOMIC_RELAXED, __HIP_MEMORY_SCOPE_AGENT); }
; #define XB_SPIN(cond, bar) do { unsigned _sp = 0; while (cond) { __builtin_amdgcn_s_sleep(1); \
;     if ((++_sp & 255u) == 0u) { if (xb_ld(&(bar)[XB_TMO])) break; if (_sp > XB_SPIN_CAP) { atomicAdd(&(bar)[XB_TMO], 1u); break; } } } } while (0)
; __device__ __forceinline__ void xcd_barrier_impl(const XcdBarrier& b, bool leader) {
;     ...
;         if (old + 1u == (gen + 1u) * nloc) {
;             __builtin_amdgcn_fence(__ATOMIC_RELEASE, "agent");
;             asm volatile("s_waitcnt vmcnt(0)" ::: "memory");
;             const unsigned og = xb_add(&bar[XB_TOP], 1u);
;             const unsigned tg = og / nx;
;             if (og + 1u != (tg + 1u) * nx) XB_SPIN(xb_ld(&bar[XB_TOP]) < (tg + 1u) * nx, bar);
.LBB0_674:
	s_or_b64 exec, exec, s[10:11]
	s_waitcnt vmcnt(0)
	s_waitcnt vmcnt(0)
.LBB0_675:
	s_andn2_saveexec_b64 s[0:1], s[8:9]
	s_cbranch_execz .LBB0_692
	s_mov_b64 s[10:11], exec
	s_waitcnt lgkmcnt(0)
	s_waitcnt vmcnt(0)
	v_mbcnt_lo_u32_b32 v2, s10, 0
	s_add_u32 s8, s6, 0x7400
	v_mbcnt_hi_u32_b32 v2, s11, v2
	s_addc_u32 s9, s7, 0
	v_cmp_eq_u32_e32 vcc, 0, v2
	s_and_saveexec_b64 s[12:13], vcc
	s_cbranch_execz .LBB0_678
	s_bcnt1_i32_b64 s0, s[10:11]
	v_mov_b32_e32 v3, s0
	global_atomic_add v3, v1, v3, s[8:9] sc0

; __device__ __forceinline__ void st16_wt(void* p, u32x4 v) { asm volatile("global_store_dwordx4 %0, %1, off sc1\n\ts_nop 1" :: "v"(p), "v"(v) : "memory"); }
; __device__ __forceinline__ unsigned cvt_pk_bf16(float lo, float hi) { unsigned r; asm volatile("v_cvt_pk_bf16_f32 %0, %1, %2" : "=v"(r) : "v"(lo), "v"(hi)); return r; }
;     __device__ __forceinline__ void operator()(const Acc& acc, const Unit& u, int wr, int wc, int fr, int fq, const LAS float* tab) const {
;     ...
;                 const size_t row = (size_t)u.pm * BM + ai * HALF + wr * 64 + m * 16 + fr; const size_t off = row * D + col0; float ss = 0.f;
; #pragma unroll
;                 for (int bj = 0; bj < 2; ++bj) { f32x4 b0, b1;
;                     if (base32) { b0 = __builtin_nontemporal_load((const f32x4*)(base32 + off + bj * HALF)); b1 = __builtin_nontemporal_load((const f32x4*)(base32 + off + bj * HALF + 4)); }
;                     else { const u32x4 b4 = rb[ai][m][bj];
;                         b0 = (f32x4){__uint_as_float(b4.x << 16), __uint_as_float(b4.x & 0xFFFF0000u), __uint_as_float(b4.y << 16), __uint_as_float(b4.y & 0xFFFF0000u)};
;                         b1 = (f32x4){__uint_as_float(b4.z << 16), __uint_as_float(b4.z & 0xFFFF0000u), __uint_as_float(b4.w << 16), __uint_as_float(b4.w & 0xFFFF0000u)}; }
;                     const f32x4 o0 = b0 + acc[ai][bj][m][0], o1 = b1 + acc[ai][bj][m][1];
;                     if (out32) {
;                         if (!dry) { *(f32x4*)(out32 + off + bj * HALF) = o0; *(f32x4*)(out32 + off + bj * HALF + 4) = o1; }
;                         continue; }
;                     ss += ((o0[0] * o0[0] + o0[1] * o0[1]) + (o0[2] * o0[2] + o0[3] * o0[3])) + ((o1[0] * o1[0] + o1[1] * o1[1]) + (o1[2] * o1[2] + o1[3] * o1[3]));
;                     u32x4 w; w.x = cvt_pk_bf16(o0[0], o0[1]); w.y = cvt_pk_bf16(o0[2], o0[3]); w.z = cvt_pk_bf16(o1[0], o1[1]); w.w = cvt_pk_bf16(o1[2], o1[3]);
;                     if (!dry) st16_wt(xb + off + bj * HALF, w); }
;                 if (out32) continue;
;                 ss = sum_rows4(ss);
;                 if (fq == 0 && !dry) ssp[row * 16 + u.pn * 4 + wc] = ss;
.LBB0_1872:
	s_waitcnt vmcnt(0)
	v_pk_add_f32 v[152:153], v[152:153], v[160:161]
	v_pk_add_f32 v[150:151], v[150:151], v[158:159]
	v_mul_f32_e32 v186, v197, v197
	v_mul_f32_e32 v187, v193, v193
	v_pk_add_f32 v[158:159], v[148:149], v[164:165]
	v_pk_add_f32 v[148:149], v[146:147], v[162:163]
	v_mul_f32_e32 v146, v151, v151
	v_mul_f32_e32 v147, v153, v153
	v_fmac_f32_e32 v186, v196, v196
	v_fmac_f32_e32 v187, v192, v192
	v_fmac_f32_e32 v146, v150, v150
	v_fmac_f32_e32 v147, v152, v152
	v_add_f32_e32 v186, v186, v187
	v_mul_f32_e32 v187, v199, v199
	v_mul_f32_e32 v188, v195, v195
	s_lshl_b32 s0, s30, 2
	v_add_f32_e32 v146, v146, v147
	v_mul_f32_e32 v147, v149, v149
	v_mul_f32_e32 v160, v159, v159
	v_fmac_f32_e32 v187, v198, v198
	v_fmac_f32_e32 v188, v194, v194
	s_ashr_i32 s1, s0, 31
	v_fmac_f32_e32 v147, v148, v148
	v_fmac_f32_e32 v160, v158, v158
	v_add_f32_e32 v187, v187, v188
	s_lshl_b64 s[0:1], s[0:1], 2
	v_add_f32_e32 v147, v147, v160
	v_add_f32_e32 v186, v186, v187
	s_add_u32 s30, s53, s0
	v_add_f32_e32 v146, v146, v147
	s_addc_u32 s31, s54, s1
	v_add_f32_e32 v160, v186, v146
	v_cvt_pk_bf16_f32 v146, v150, v151
	s_mov_b64 s[0:1], 0x100
	v_cvt_pk_bf16_f32 v147, v152, v153
	v_cvt_pk_bf16_f32 v148, v148, v149
	v_cvt_pk_bf16_f32 v149, v158, v159
	v_lshl_add_u64 v[150:151], v[190:191], 0, s[0:1]
	global_store_dwordx4 v[150:151], v[146:149], off sc1
	s_nop 1
	v_mov_b32_e32 v146, v160
	s_nop 1
	v_permlane16_swap_b32_e32 v160, v146
	v_add_f32_e32 v146, v160, v146
	v_mov_b32_e32 v147, v146
	s_nop 1
	v_permlane32_swap_b32_e32 v146, v147
	s_and_saveexec_b64 s[34:35], s[4:5]
	s_cbranch_execz .LBB0_1874
	v_add_f32_e32 v148, v146, v147
	v_lshlrev_b64 v[146:147], 6, v[220:221]
	v_lshl_add_u64 v[146:147], s[30:31], 0, v[146:147]
	global_store_dword v[146:147], v148, off sc1

; __device__ __forceinline__ void st16_wt(void* p, u32x4 v) { asm volatile("global_store_dwordx4 %0, %1, off sc1\n\ts_nop 1" :: "v"(p), "v"(v) : "memory"); }
; __device__ __forceinline__ unsigned cvt_pk_bf16(float lo, float hi) { unsigned r; asm volatile("v_cvt_pk_bf16_f32 %0, %1, %2" : "=v"(r) : "v"(lo), "v"(hi)); return r; }
;     __device__ __forceinline__ void operator()(const Acc& acc, const Unit& u, int wr, int wc, int fr, int fq, const LAS float* tab) const {
;     ...
;                 const size_t row = (size_t)u.pm * BM + ai * HALF + wr * 64 + m * 16 + fr; const size_t off = row * D + col0; float ss = 0.f;
; #pragma unroll
;                 for (int bj = 0; bj < 2; ++bj) { f32x4 b0, b1;
;                     if (base32) { b0 = __builtin_nontemporal_load((const f32x4*)(base32 + off + bj * HALF)); b1 = __builtin_nontemporal_load((const f32x4*)(base32 + off + bj * HALF + 4)); }
;                     else { const u32x4 b4 = rb[ai][m][bj];
;                         b0 = (f32x4){__uint_as_float(b4.x << 16), __uint_as_float(b4.x & 0xFFFF0000u), __uint_as_float(b4.y << 16), __uint_as_float(b4.y & 0xFFFF0000u)};
;                         b1 = (f32x4){__uint_as_float(b4.z << 16), __uint_as_float(b4.z & 0xFFFF0000u), __uint_as_float(b4.w << 16), __uint_as_float(b4.w & 0xFFFF0000u)}; }
;                     const f32x4 o0 = b0 + acc[ai][bj][m][0], o1 = b1 + acc[ai][bj][m][1];
;                     if (out32) {
;                         if (!dry) { *(f32x4*)(out32 + off + bj * HALF) = o0; *(f32x4*)(out32 + off + bj * HALF + 4) = o1; }
;                         continue; }
;                     ss += ((o0[0] * o0[0] + o0[1] * o0[1]) + (o0[2] * o0[2] + o0[3] * o0[3])) + ((o1[0] * o1[0] + o1[1] * o1[1]) + (o1[2] * o1[2] + o1[3] * o1[3]));
;                     u32x4 w; w.x = cvt_pk_bf16(o0[0], o0[1]); w.y = cvt_pk_bf16(o0[2], o0[3]); w.z = cvt_pk_bf16(o1[0], o1[1]); w.w = cvt_pk_bf16(o1[2], o1[3]);
;                     if (!dry) st16_wt(xb + off + bj * HALF, w); }
;                 if (out32) continue;
;                 ss = sum_rows4(ss);
;                 if (fq == 0 && !dry) ssp[row * 16 + u.pn * 4 + wc] = ss;
.LBB0_1882:
	s_waitcnt vmcnt(0)
	v_pk_add_f32 v[128:129], v[128:129], v[132:133]
	v_pk_add_f32 v[126:127], v[126:127], v[130:131]
	v_mul_f32_e32 v152, v165, v165
	v_mul_f32_e32 v149, v149, v149
	v_pk_add_f32 v[130:131], v[120:121], v[136:137]
	v_pk_add_f32 v[120:121], v[118:119], v[134:135]
	v_mul_f32_e32 v118, v127, v127
	v_mul_f32_e32 v119, v129, v129
	v_fmac_f32_e32 v152, v164, v164
	v_fmac_f32_e32 v149, v148, v148
	v_fmac_f32_e32 v118, v126, v126
	v_fmac_f32_e32 v119, v128, v128
	v_add_f32_e32 v148, v152, v149
	v_mul_f32_e32 v149, v151, v151
	v_mul_f32_e32 v147, v147, v147
	v_add_f32_e32 v118, v118, v119
	v_mul_f32_e32 v119, v121, v121
	v_mul_f32_e32 v132, v131, v131
	v_fmac_f32_e32 v149, v150, v150
	v_fmac_f32_e32 v147, v146, v146
	v_fmac_f32_e32 v119, v120, v120
	v_fmac_f32_e32 v132, v130, v130
	v_add_f32_e32 v146, v149, v147
	v_add_f32_e32 v119, v119, v132
	v_add_f32_e32 v146, v148, v146
	v_add_f32_e32 v118, v118, v119
	v_add_f32_e32 v132, v146, v118
	v_cvt_pk_bf16_f32 v118, v126, v127
	v_cvt_pk_bf16_f32 v119, v128, v129
	v_cvt_pk_bf16_f32 v120, v120, v121
	v_cvt_pk_bf16_f32 v121, v130, v131
	v_lshl_add_u64 v[126:127], v[160:161], 0, s[0:1]
	global_store_dwordx4 v[126:127], v[118:121], off sc1
	s_nop 1
	v_mov_b32_e32 v118, v132
	s_nop 1
	v_permlane16_swap_b32_e32 v132, v118
	v_add_f32_e32 v118, v132, v118
	v_mov_b32_e32 v119, v118
	s_nop 1
	v_permlane32_swap_b32_e32 v118, v119
	s_and_saveexec_b64 s[34:35], s[4:5]
	s_cbranch_execz .LBB0_1884
	v_add_f32_e32 v120, v118, v119
	v_lshlrev_b64 v[118:119], 6, v[158:159]
	v_lshl_add_u64 v[118:119], s[30:31], 0, v[118:119]
	global_store_dword v[118:119], v120, off sc1

; __device__ __forceinline__ void st16_wt(void* p, u32x4 v) { asm volatile("global_store_dwordx4 %0, %1, off sc1\n\ts_nop 1" :: "v"(p), "v"(v) : "memory"); }
; __device__ __forceinline__ unsigned cvt_pk_bf16(float lo, float hi) { unsigned r; asm volatile("v_cvt_pk_bf16_f32 %0, %1, %2" : "=v"(r) : "v"(lo), "v"(hi)); return r; }
;     __device__ __forceinline__ void operator()(const Acc& acc, const Unit& u, int wr, int wc, int fr, int fq, const LAS float* tab) const {
;     ...
;                 const size_t row = (size_t)u.pm * BM + ai * HALF + wr * 64 + m * 16 + fr; const size_t off = row * D + col0; float ss = 0.f;
; #pragma unroll
;                 for (int bj = 0; bj < 2; ++bj) { f32x4 b0, b1;
;                     if (base32) { b0 = __builtin_nontemporal_load((const f32x4*)(base32 + off + bj * HALF)); b1 = __builtin_nontemporal_load((const f32x4*)(base32 + off + bj * HALF + 4)); }
;                     else { const u32x4 b4 = rb[ai][m][bj];
;                         b0 = (f32x4){__uint_as_float(b4.x << 16), __uint_as_float(b4.x & 0xFFFF0000u), __uint_as_float(b4.y << 16), __uint_as_float(b4.y & 0xFFFF0000u)};
;                         b1 = (f32x4){__uint_as_float(b4.z << 16), __uint_as_float(b4.z & 0xFFFF0000u), __uint_as_float(b4.w << 16), __uint_as_float(b4.w & 0xFFFF0000u)}; }
;                     const f32x4 o0 = b0 + acc[ai][bj][m][0], o1 = b1 + acc[ai][bj][m][1];
;                     if (out32) {
;                         if (!dry) { *(f32x4*)(out32 + off + bj * HALF) = o0; *(f32x4*)(out32 + off + bj * HALF + 4) = o1; }
;                         continue; }
;                     ss += ((o0[0] * o0[0] + o0[1] * o0[1]) + (o0[2] * o0[2] + o0[3] * o0[3])) + ((o1[0] * o1[0] + o1[1] * o1[1]) + (o1[2] * o1[2] + o1[3] * o1[3]));
;                     u32x4 w; w.x = cvt_pk_bf16(o0[0], o0[1]); w.y = cvt_pk_bf16(o0[2], o0[3]); w.z = cvt_pk_bf16(o1[0], o1[1]); w.w = cvt_pk_bf16(o1[2], o1[3]);
;                     if (!dry) st16_wt(xb + off + bj * HALF, w); }
;                 if (out32) continue;
;                 ss = sum_rows4(ss);
;                 if (fq == 0 && !dry) ssp[row * 16 + u.pn * 4 + wc] = ss;
.LBB0_1892:
	s_waitcnt vmcnt(0)
	v_pk_add_f32 v[100:101], v[100:101], v[108:109]
	v_pk_add_f32 v[98:99], v[98:99], v[106:107]
	v_mul_f32_e32 v128, v137, v137
	v_mul_f32_e32 v121, v121, v121
	v_pk_add_f32 v[106:107], v[96:97], v[112:113]
	v_pk_add_f32 v[96:97], v[94:95], v[110:111]
	v_mul_f32_e32 v94, v99, v99
	v_mul_f32_e32 v95, v101, v101
	v_fmac_f32_e32 v128, v136, v136
	v_fmac_f32_e32 v121, v120, v120
	v_fmac_f32_e32 v94, v98, v98
	v_fmac_f32_e32 v95, v100, v100
	v_add_f32_e32 v120, v128, v121
	v_mul_f32_e32 v121, v127, v127
	v_mul_f32_e32 v119, v119, v119
	v_add_f32_e32 v94, v94, v95
	v_mul_f32_e32 v95, v97, v97
	v_mul_f32_e32 v108, v107, v107
	v_fmac_f32_e32 v121, v126, v126
	v_fmac_f32_e32 v119, v118, v118
	v_fmac_f32_e32 v95, v96, v96
	v_fmac_f32_e32 v108, v106, v106
	v_add_f32_e32 v118, v121, v119
	v_add_f32_e32 v95, v95, v108
	v_add_f32_e32 v118, v120, v118
	v_add_f32_e32 v94, v94, v95
	v_add_f32_e32 v108, v118, v94
	v_cvt_pk_bf16_f32 v94, v98, v99
	v_cvt_pk_bf16_f32 v95, v100, v101
	v_cvt_pk_bf16_f32 v96, v96, v97
	v_cvt_pk_bf16_f32 v97, v106, v107
	v_lshl_add_u64 v[98:99], v[132:133], 0, s[0:1]
	global_store_dwordx4 v[98:99], v[94:97], off sc1
	s_nop 1
	v_mov_b32_e32 v94, v108
	s_nop 1
	v_permlane16_swap_b32_e32 v108, v94
	v_add_f32_e32 v94, v108, v94
	v_mov_b32_e32 v95, v94
	s_nop 1
	v_permlane32_swap_b32_e32 v94, v95
	s_and_saveexec_b64 s[34:35], s[4:5]
	s_cbranch_execz .LBB0_1894
	v_add_f32_e32 v96, v94, v95
	v_lshlrev_b64 v[94:95], 6, v[130:131]
	v_lshl_add_u64 v[94:95], s[30:31], 0, v[94:95]
	global_store_dword v[94:95], v96, off sc1

; __device__ __forceinline__ void st16_wt(void* p, u32x4 v) { asm volatile("global_store_dwordx4 %0, %1, off sc1\n\ts_nop 1" :: "v"(p), "v"(v) : "memory"); }
; __device__ __forceinline__ unsigned cvt_pk_bf16(float lo, float hi) { unsigned r; asm volatile("v_cvt_pk_bf16_f32 %0, %1, %2" : "=v"(r) : "v"(lo), "v"(hi)); return r; }
;     __device__ __forceinline__ void operator()(const Acc& acc, const Unit& u, int wr, int wc, int fr, int fq, const LAS float* tab) const {
;     ...
;                 const size_t row = (size_t)u.pm * BM + ai * HALF + wr * 64 + m * 16 + fr; const size_t off = row * D + col0; float ss = 0.f;
; #pragma unroll
;                 for (int bj = 0; bj < 2; ++bj) { f32x4 b0, b1;
;                     if (base32) { b0 = __builtin_nontemporal_load((const f32x4*)(base32 + off + bj * HALF)); b1 = __builtin_nontemporal_load((const f32x4*)(base32 + off + bj * HALF + 4)); }
;                     else { const u32x4 b4 = rb[ai][m][bj];
;                         b0 = (f32x4){__uint_as_float(b4.x << 16), __uint_as_float(b4.x & 0xFFFF0000u), __uint_as_float(b4.y << 16), __uint_as_float(b4.y & 0xFFFF0000u)};
;                         b1 = (f32x4){__uint_as_float(b4.z << 16), __uint_as_float(b4.z & 0xFFFF0000u), __uint_as_float(b4.w << 16), __uint_as_float(b4.w & 0xFFFF0000u)}; }
;                     const f32x4 o0 = b0 + acc[ai][bj][m][0], o1 = b1 + acc[ai][bj][m][1];
;                     if (out32) {
;                         if (!dry) { *(f32x4*)(out32 + off + bj * HALF) = o0; *(f32x4*)(out32 + off + bj * HALF + 4) = o1; }
;                         continue; }
;                     ss += ((o0[0] * o0[0] + o0[1] * o0[1]) + (o0[2] * o0[2] + o0[3] * o0[3])) + ((o1[0] * o1[0] + o1[1] * o1[1]) + (o1[2] * o1[2] + o1[3] * o1[3]));
;                     u32x4 w; w.x = cvt_pk_bf16(o0[0], o0[1]); w.y = cvt_pk_bf16(o0[2], o0[3]); w.z = cvt_pk_bf16(o1[0], o1[1]); w.w = cvt_pk_bf16(o1[2], o1[3]);
;                     if (!dry) st16_wt(xb + off + bj * HALF, w); }
;                 if (out32) continue;
;                 ss = sum_rows4(ss);
;                 if (fq == 0 && !dry) ssp[row * 16 + u.pn * 4 + wc] = ss;
.LBB0_1902:
	s_waitcnt vmcnt(0)
	v_pk_add_f32 v[76:77], v[76:77], v[84:85]
	v_pk_add_f32 v[74:75], v[74:75], v[82:83]
	v_mul_f32_e32 v100, v113, v113
	v_mul_f32_e32 v97, v97, v97
	v_pk_add_f32 v[82:83], v[72:73], v[88:89]
	v_pk_add_f32 v[72:73], v[70:71], v[86:87]
	v_mul_f32_e32 v70, v75, v75
	v_mul_f32_e32 v71, v77, v77
	v_fmac_f32_e32 v100, v112, v112
	v_fmac_f32_e32 v97, v96, v96
	v_fmac_f32_e32 v70, v74, v74
	v_fmac_f32_e32 v71, v76, v76
	v_add_f32_e32 v96, v100, v97
	v_mul_f32_e32 v97, v99, v99
	v_mul_f32_e32 v95, v95, v95
	v_add_f32_e32 v70, v70, v71
	v_mul_f32_e32 v71, v73, v73
	v_mul_f32_e32 v84, v83, v83
	v_fmac_f32_e32 v97, v98, v98
	v_fmac_f32_e32 v95, v94, v94
	v_fmac_f32_e32 v71, v72, v72
	v_fmac_f32_e32 v84, v82, v82
	v_add_f32_e32 v94, v97, v95
	v_add_f32_e32 v71, v71, v84
	v_add_f32_e32 v94, v96, v94
	v_add_f32_e32 v70, v70, v71
	v_add_f32_e32 v84, v94, v70
	v_cvt_pk_bf16_f32 v70, v74, v75
	v_cvt_pk_bf16_f32 v71, v76, v77
	v_cvt_pk_bf16_f32 v72, v72, v73
	v_cvt_pk_bf16_f32 v73, v82, v83
	v_lshl_add_u64 v[74:75], v[108:109], 0, s[0:1]
	global_store_dwordx4 v[74:75], v[70:73], off sc1
	s_nop 1
	v_mov_b32_e32 v70, v84
	s_nop 1
	v_permlane16_swap_b32_e32 v84, v70
	v_add_f32_e32 v70, v84, v70
	v_mov_b32_e32 v71, v70
	s_nop 1
	v_permlane32_swap_b32_e32 v70, v71
	s_and_saveexec_b64 s[34:35], s[4:5]
	s_cbranch_execz .LBB0_1904
	v_add_f32_e32 v72, v70, v71
	v_lshlrev_b64 v[70:71], 6, v[106:107]
	v_lshl_add_u64 v[70:71], s[30:31], 0, v[70:71]
	global_store_dword v[70:71], v72, off sc1

; __device__ __forceinline__ void st16_wt(void* p, u32x4 v) { asm volatile("global_store_dwordx4 %0, %1, off sc1\n\ts_nop 1" :: "v"(p), "v"(v) : "memory"); }
; __device__ __forceinline__ unsigned cvt_pk_bf16(float lo, float hi) { unsigned r; asm volatile("v_cvt_pk_bf16_f32 %0, %1, %2" : "=v"(r) : "v"(lo), "v"(hi)); return r; }
;     __device__ __forceinline__ void operator()(const Acc& acc, const Unit& u, int wr, int wc, int fr, int fq, const LAS float* tab) const {
;     ...
;                 const size_t row = (size_t)u.pm * BM + ai * HALF + wr * 64 + m * 16 + fr; const size_t off = row * D + col0; float ss = 0.f;
; #pragma unroll
;                 for (int bj = 0; bj < 2; ++bj) { f32x4 b0, b1;
;                     if (base32) { b0 = __builtin_nontemporal_load((const f32x4*)(base32 + off + bj * HALF)); b1 = __builtin_nontemporal_load((const f32x4*)(base32 + off + bj * HALF + 4)); }
;                     else { const u32x4 b4 = rb[ai][m][bj];
;                         b0 = (f32x4){__uint_as_float(b4.x << 16), __uint_as_float(b4.x & 0xFFFF0000u), __uint_as_float(b4.y << 16), __uint_as_float(b4.y & 0xFFFF0000u)};
;                         b1 = (f32x4){__uint_as_float(b4.z << 16), __uint_as_float(b4.z & 0xFFFF0000u), __uint_as_float(b4.w << 16), __uint_as_float(b4.w & 0xFFFF0000u)}; }
;                     const f32x4 o0 = b0 + acc[ai][bj][m][0], o1 = b1 + acc[ai][bj][m][1];
;                     if (out32) {
;                         if (!dry) { *(f32x4*)(out32 + off + bj * HALF) = o0; *(f32x4*)(out32 + off + bj * HALF + 4) = o1; }
;                         continue; }
;                     ss += ((o0[0] * o0[0] + o0[1] * o0[1]) + (o0[2] * o0[2] + o0[3] * o0[3])) + ((o1[0] * o1[0] + o1[1] * o1[1]) + (o1[2] * o1[2] + o1[3] * o1[3]));
;                     u32x4 w; w.x = cvt_pk_bf16(o0[0], o0[1]); w.y = cvt_pk_bf16(o0[2], o0[3]); w.z = cvt_pk_bf16(o1[0], o1[1]); w.w = cvt_pk_bf16(o1[2], o1[3]);
;                     if (!dry) st16_wt(xb + off + bj * HALF, w); }
;                 if (out32) continue;
;                 ss = sum_rows4(ss);
;                 if (fq == 0 && !dry) ssp[row * 16 + u.pn * 4 + wc] = ss;
.LBB0_1912:
	s_waitcnt vmcnt(0)
	v_pk_add_f32 v[56:57], v[56:57], v[60:61]
	v_pk_add_f32 v[54:55], v[54:55], v[58:59]
	v_mul_f32_e32 v76, v89, v89
	v_mul_f32_e32 v73, v73, v73
	v_pk_add_f32 v[58:59], v[52:53], v[64:65]
	v_pk_add_f32 v[52:53], v[50:51], v[62:63]
	v_mul_f32_e32 v50, v55, v55
	v_mul_f32_e32 v51, v57, v57
	v_fmac_f32_e32 v76, v88, v88
	v_fmac_f32_e32 v73, v72, v72
	v_fmac_f32_e32 v50, v54, v54
	v_fmac_f32_e32 v51, v56, v56
	v_add_f32_e32 v72, v76, v73
	v_mul_f32_e32 v73, v75, v75
	v_mul_f32_e32 v71, v71, v71
	v_add_f32_e32 v50, v50, v51
	v_mul_f32_e32 v51, v53, v53
	v_mul_f32_e32 v60, v59, v59
	v_fmac_f32_e32 v73, v74, v74
	v_fmac_f32_e32 v71, v70, v70
	v_fmac_f32_e32 v51, v52, v52
	v_fmac_f32_e32 v60, v58, v58
	v_add_f32_e32 v70, v73, v71
	v_add_f32_e32 v51, v51, v60
	v_add_f32_e32 v70, v72, v70
	v_add_f32_e32 v50, v50, v51
	v_add_f32_e32 v60, v70, v50
	v_cvt_pk_bf16_f32 v50, v54, v55
	v_cvt_pk_bf16_f32 v51, v56, v57
	v_cvt_pk_bf16_f32 v52, v52, v53
	v_cvt_pk_bf16_f32 v53, v58, v59
	v_lshl_add_u64 v[54:55], v[84:85], 0, s[0:1]
	global_store_dwordx4 v[54:55], v[50:53], off sc1
	s_nop 1
	v_mov_b32_e32 v50, v60
	s_nop 1
	v_permlane16_swap_b32_e32 v60, v50
	v_add_f32_e32 v50, v60, v50
	v_mov_b32_e32 v51, v50
	s_nop 1
	v_permlane32_swap_b32_e32 v50, v51
	s_and_saveexec_b64 s[34:35], s[4:5]
	s_cbranch_execz .LBB0_1914
	v_add_f32_e32 v52, v50, v51
	v_lshlrev_b64 v[50:51], 6, v[82:83]
	v_lshl_add_u64 v[50:51], s[30:31], 0, v[50:51]
	global_store_dword v[50:51], v52, off sc1

; __device__ __forceinline__ void st16_wt(void* p, u32x4 v) { asm volatile("global_store_dwordx4 %0, %1, off sc1\n\ts_nop 1" :: "v"(p), "v"(v) : "memory"); }
; __device__ __forceinline__ unsigned cvt_pk_bf16(float lo, float hi) { unsigned r; asm volatile("v_cvt_pk_bf16_f32 %0, %1, %2" : "=v"(r) : "v"(lo), "v"(hi)); return r; }
;     __device__ __forceinline__ void operator()(const Acc& acc, const Unit& u, int wr, int wc, int fr, int fq, const LAS float* tab) const {
;     ...
;                 const size_t row = (size_t)u.pm * BM + ai * HALF + wr * 64 + m * 16 + fr; const size_t off = row * D + col0; float ss = 0.f;
; #pragma unroll
;                 for (int bj = 0; bj < 2; ++bj) { f32x4 b0, b1;
;                     if (base32) { b0 = __builtin_nontemporal_load((const f32x4*)(base32 + off + bj * HALF)); b1 = __builtin_nontemporal_load((const f32x4*)(base32 + off + bj * HALF + 4)); }
;                     else { const u32x4 b4 = rb[ai][m][bj];
;                         b0 = (f32x4){__uint_as_float(b4.x << 16), __uint_as_float(b4.x & 0xFFFF0000u), __uint_as_float(b4.y << 16), __uint_as_float(b4.y & 0xFFFF0000u)};
;                         b1 = (f32x4){__uint_as_float(b4.z << 16), __uint_as_float(b4.z & 0xFFFF0000u), __uint_as_float(b4.w << 16), __uint_as_float(b4.w & 0xFFFF0000u)}; }
;                     const f32x4 o0 = b0 + acc[ai][bj][m][0], o1 = b1 + acc[ai][bj][m][1];
;                     if (out32) {
;                         if (!dry) { *(f32x4*)(out32 + off + bj * HALF) = o0; *(f32x4*)(out32 + off + bj * HALF + 4) = o1; }
;                         continue; }
;                     ss += ((o0[0] * o0[0] + o0[1] * o0[1]) + (o0[2] * o0[2] + o0[3] * o0[3])) + ((o1[0] * o1[0] + o1[1] * o1[1]) + (o1[2] * o1[2] + o1[3] * o1[3]));
;                     u32x4 w; w.x = cvt_pk_bf16(o0[0], o0[1]); w.y = cvt_pk_bf16(o0[2], o0[3]); w.z = cvt_pk_bf16(o1[0], o1[1]); w.w = cvt_pk_bf16(o1[2], o1[3]);
;                     if (!dry) st16_wt(xb + off + bj * HALF, w); }
;                 if (out32) continue;
;                 ss = sum_rows4(ss);
;                 if (fq == 0 && !dry) ssp[row * 16 + u.pn * 4 + wc] = ss;
.LBB0_1922:
	s_waitcnt vmcnt(0)
	v_pk_add_f32 v[40:41], v[40:41], v[44:45]
	v_pk_add_f32 v[38:39], v[38:39], v[42:43]
	v_mul_f32_e32 v56, v65, v65
	v_mul_f32_e32 v53, v53, v53
	v_pk_add_f32 v[42:43], v[36:37], v[48:49]
	v_pk_add_f32 v[36:37], v[34:35], v[46:47]
	v_mul_f32_e32 v34, v39, v39
	v_mul_f32_e32 v35, v41, v41
	v_fmac_f32_e32 v56, v64, v64
	v_fmac_f32_e32 v53, v52, v52
	v_fmac_f32_e32 v34, v38, v38
	v_fmac_f32_e32 v35, v40, v40
	v_add_f32_e32 v52, v56, v53
	v_mul_f32_e32 v53, v55, v55
	v_mul_f32_e32 v51, v51, v51
	v_add_f32_e32 v34, v34, v35
	v_mul_f32_e32 v35, v37, v37
	v_mul_f32_e32 v44, v43, v43
	v_fmac_f32_e32 v53, v54, v54
	v_fmac_f32_e32 v51, v50, v50
	v_fmac_f32_e32 v35, v36, v36
	v_fmac_f32_e32 v44, v42, v42
	v_add_f32_e32 v50, v53, v51
	v_add_f32_e32 v35, v35, v44
	v_add_f32_e32 v50, v52, v50
	v_add_f32_e32 v34, v34, v35
	v_add_f32_e32 v44, v50, v34
	v_cvt_pk_bf16_f32 v34, v38, v39
	s_mov_b64 s[0:1], 0x100
	v_cvt_pk_bf16_f32 v35, v40, v41
	v_cvt_pk_bf16_f32 v36, v36, v37
	v_cvt_pk_bf16_f32 v37, v42, v43
	v_lshl_add_u64 v[38:39], v[60:61], 0, s[0:1]
	global_store_dwordx4 v[38:39], v[34:37], off sc1
	s_nop 1
	v_mov_b32_e32 v34, v44
	s_nop 1
	v_permlane16_swap_b32_e32 v44, v34
	v_add_f32_e32 v34, v44, v34
	v_mov_b32_e32 v35, v34
	s_nop 1
	v_permlane32_swap_b32_e32 v34, v35
	s_and_saveexec_b64 s[34:35], s[4:5]
	s_cbranch_execz .LBB0_1924
	v_add_f32_e32 v36, v34, v35
	v_lshlrev_b64 v[34:35], 6, v[58:59]
	v_lshl_add_u64 v[34:35], s[30:31], 0, v[34:35]
	global_store_dword v[34:35], v36, off sc1

; __device__ __forceinline__ void st16_wt(void* p, u32x4 v) { asm volatile("global_store_dwordx4 %0, %1, off sc1\n\ts_nop 1" :: "v"(p), "v"(v) : "memory"); }
; __device__ __forceinline__ unsigned cvt_pk_bf16(float lo, float hi) { unsigned r; asm volatile("v_cvt_pk_bf16_f32 %0, %1, %2" : "=v"(r) : "v"(lo), "v"(hi)); return r; }
;     __device__ __forceinline__ void operator()(const Acc& acc, const Unit& u, int wr, int wc, int fr, int fq, const LAS float* tab) const {
;     ...
;                 const size_t row = (size_t)u.pm * BM + ai * HALF + wr * 64 + m * 16 + fr; const size_t off = row * D + col0; float ss = 0.f;
; #pragma unroll
;                 for (int bj = 0; bj < 2; ++bj) { f32x4 b0, b1;
;                     if (base32) { b0 = __builtin_nontemporal_load((const f32x4*)(base32 + off + bj * HALF)); b1 = __builtin_nontemporal_load((const f32x4*)(base32 + off + bj * HALF + 4)); }
;                     else { const u32x4 b4 = rb[ai][m][bj];
;                         b0 = (f32x4){__uint_as_float(b4.x << 16), __uint_as_float(b4.x & 0xFFFF0000u), __uint_as_float(b4.y << 16), __uint_as_float(b4.y & 0xFFFF0000u)};
;                         b1 = (f32x4){__uint_as_float(b4.z << 16), __uint_as_float(b4.z & 0xFFFF0000u), __uint_as_float(b4.w << 16), __uint_as_float(b4.w & 0xFFFF0000u)}; }
;                     const f32x4 o0 = b0 + acc[ai][bj][m][0], o1 = b1 + acc[ai][bj][m][1];
;                     if (out32) {
;                         if (!dry) { *(f32x4*)(out32 + off + bj * HALF) = o0; *(f32x4*)(out32 + off + bj * HALF + 4) = o1; }
;                         continue; }
;                     ss += ((o0[0] * o0[0] + o0[1] * o0[1]) + (o0[2] * o0[2] + o0[3] * o0[3])) + ((o1[0] * o1[0] + o1[1] * o1[1]) + (o1[2] * o1[2] + o1[3] * o1[3]));
;                     u32x4 w; w.x = cvt_pk_bf16(o0[0], o0[1]); w.y = cvt_pk_bf16(o0[2], o0[3]); w.z = cvt_pk_bf16(o1[0], o1[1]); w.w = cvt_pk_bf16(o1[2], o1[3]);
;                     if (!dry) st16_wt(xb + off + bj * HALF, w); }
;                 if (out32) continue;
;                 ss = sum_rows4(ss);
;                 if (fq == 0 && !dry) ssp[row * 16 + u.pn * 4 + wc] = ss;
.LBB0_1932:
	s_waitcnt vmcnt(0)
	v_pk_add_f32 v[24:25], v[24:25], v[28:29]
	v_pk_add_f32 v[22:23], v[22:23], v[26:27]
	v_mul_f32_e32 v40, v49, v49
	v_mul_f32_e32 v37, v37, v37
	v_pk_add_f32 v[26:27], v[20:21], v[32:33]
	v_pk_add_f32 v[20:21], v[18:19], v[30:31]
	v_mul_f32_e32 v18, v23, v23
	v_mul_f32_e32 v19, v25, v25
	v_fmac_f32_e32 v40, v48, v48
	v_fmac_f32_e32 v37, v36, v36
	v_fmac_f32_e32 v18, v22, v22
	v_fmac_f32_e32 v19, v24, v24
	v_add_f32_e32 v36, v40, v37
	v_mul_f32_e32 v37, v39, v39
	v_mul_f32_e32 v35, v35, v35
	v_add_f32_e32 v18, v18, v19
	v_mul_f32_e32 v19, v21, v21
	v_mul_f32_e32 v28, v27, v27
	v_fmac_f32_e32 v37, v38, v38
	v_fmac_f32_e32 v35, v34, v34
	v_fmac_f32_e32 v19, v20, v20
	v_fmac_f32_e32 v28, v26, v26
	v_add_f32_e32 v34, v37, v35
	v_add_f32_e32 v19, v19, v28
	v_add_f32_e32 v34, v36, v34
	v_add_f32_e32 v18, v18, v19
	v_add_f32_e32 v28, v34, v18
	v_cvt_pk_bf16_f32 v18, v22, v23
	s_mov_b64 s[0:1], 0x100
	v_cvt_pk_bf16_f32 v19, v24, v25
	v_cvt_pk_bf16_f32 v20, v20, v21
	v_cvt_pk_bf16_f32 v21, v26, v27
	v_lshl_add_u64 v[22:23], v[44:45], 0, s[0:1]
	global_store_dwordx4 v[22:23], v[18:21], off sc1
	s_nop 1
	v_mov_b32_e32 v18, v28
	s_nop 1
	v_permlane16_swap_b32_e32 v28, v18
	v_add_f32_e32 v18, v28, v18
	v_mov_b32_e32 v19, v18
	s_nop 1
	v_permlane32_swap_b32_e32 v18, v19
	s_and_saveexec_b64 s[34:35], s[4:5]
	s_cbranch_execz .LBB0_1934
	v_add_f32_e32 v20, v18, v19
	v_lshlrev_b64 v[18:19], 6, v[42:43]
	v_lshl_add_u64 v[18:19], s[30:31], 0, v[18:19]
	global_store_dword v[18:19], v20, off sc1

; __device__ __forceinline__ void st16_wt(void* p, u32x4 v) { asm volatile("global_store_dwordx4 %0, %1, off sc1\n\ts_nop 1" :: "v"(p), "v"(v) : "memory"); }
; __device__ __forceinline__ unsigned cvt_pk_bf16(float lo, float hi) { unsigned r; asm volatile("v_cvt_pk_bf16_f32 %0, %1, %2" : "=v"(r) : "v"(lo), "v"(hi)); return r; }
;     __device__ __forceinline__ void operator()(const Acc& acc, const Unit& u, int wr, int wc, int fr, int fq, const LAS float* tab) const {
;     ...
;                 const size_t row = (size_t)u.pm * BM + ai * HALF + wr * 64 + m * 16 + fr; const size_t off = row * D + col0; float ss = 0.f;
; #pragma unroll
;                 for (int bj = 0; bj < 2; ++bj) { f32x4 b0, b1;
;                     if (base32) { b0 = __builtin_nontemporal_load((const f32x4*)(base32 + off + bj * HALF)); b1 = __builtin_nontemporal_load((const f32x4*)(base32 + off + bj * HALF + 4)); }
;                     else { const u32x4 b4 = rb[ai][m][bj];
;                         b0 = (f32x4){__uint_as_float(b4.x << 16), __uint_as_float(b4.x & 0xFFFF0000u), __uint_as_float(b4.y << 16), __uint_as_float(b4.y & 0xFFFF0000u)};
;                         b1 = (f32x4){__uint_as_float(b4.z << 16), __uint_as_float(b4.z & 0xFFFF0000u), __uint_as_float(b4.w << 16), __uint_as_float(b4.w & 0xFFFF0000u)}; }
;                     const f32x4 o0 = b0 + acc[ai][bj][m][0], o1 = b1 + acc[ai][bj][m][1];
;                     if (out32) {
;                         if (!dry) { *(f32x4*)(out32 + off + bj * HALF) = o0; *(f32x4*)(out32 + off + bj * HALF + 4) = o1; }
;                         continue; }
;                     ss += ((o0[0] * o0[0] + o0[1] * o0[1]) + (o0[2] * o0[2] + o0[3] * o0[3])) + ((o1[0] * o1[0] + o1[1] * o1[1]) + (o1[2] * o1[2] + o1[3] * o1[3]));
;                     u32x4 w; w.x = cvt_pk_bf16(o0[0], o0[1]); w.y = cvt_pk_bf16(o0[2], o0[3]); w.z = cvt_pk_bf16(o1[0], o1[1]); w.w = cvt_pk_bf16(o1[2], o1[3]);
;                     if (!dry) st16_wt(xb + off + bj * HALF, w); }
;                 if (out32) continue;
;                 ss = sum_rows4(ss);
;                 if (fq == 0 && !dry) ssp[row * 16 + u.pn * 4 + wc] = ss;
.LBB0_1942:
	s_waitcnt vmcnt(0)
	v_pk_add_f32 v[8:9], v[8:9], v[12:13]
	v_pk_add_f32 v[6:7], v[6:7], v[10:11]
	v_mul_f32_e32 v24, v33, v33
	v_mul_f32_e32 v21, v21, v21
	v_pk_add_f32 v[10:11], v[4:5], v[16:17]
	v_pk_add_f32 v[4:5], v[2:3], v[14:15]
	v_mul_f32_e32 v2, v7, v7
	v_mul_f32_e32 v3, v9, v9
	v_fmac_f32_e32 v24, v32, v32
	v_fmac_f32_e32 v21, v20, v20
	v_fmac_f32_e32 v2, v6, v6
	v_fmac_f32_e32 v3, v8, v8
	v_add_f32_e32 v20, v24, v21
	v_mul_f32_e32 v21, v23, v23
	v_mul_f32_e32 v19, v19, v19
	v_add_f32_e32 v2, v2, v3
	v_mul_f32_e32 v3, v5, v5
	v_mul_f32_e32 v12, v11, v11
	v_fmac_f32_e32 v21, v22, v22
	v_fmac_f32_e32 v19, v18, v18
	v_fmac_f32_e32 v3, v4, v4
	v_fmac_f32_e32 v12, v10, v10
	v_add_f32_e32 v18, v21, v19
	v_add_f32_e32 v3, v3, v12
	v_add_f32_e32 v18, v20, v18
	v_add_f32_e32 v2, v2, v3
	v_add_f32_e32 v12, v18, v2
	v_cvt_pk_bf16_f32 v2, v6, v7
	s_mov_b64 s[0:1], 0x100
	v_cvt_pk_bf16_f32 v3, v8, v9
	v_cvt_pk_bf16_f32 v4, v4, v5
	v_cvt_pk_bf16_f32 v5, v10, v11
	v_lshl_add_u64 v[6:7], v[28:29], 0, s[0:1]
	global_store_dwordx4 v[6:7], v[2:5], off sc1
	s_nop 1
	v_mov_b32_e32 v2, v12
	s_nop 1
	v_permlane16_swap_b32_e32 v12, v2
	v_add_f32_e32 v2, v12, v2
	v_mov_b32_e32 v3, v2
	s_nop 1
	v_permlane32_swap_b32_e32 v2, v3
	s_and_saveexec_b64 s[8:9], s[4:5]
	s_cbranch_execz .LBB0_1944
	v_add_f32_e32 v4, v2, v3
	v_lshlrev_b64 v[2:3], 6, v[26:27]
	v_lshl_add_u64 v[2:3], s[30:31], 0, v[2:3]
	global_store_dword v[2:3], v4, off sc1

;     __device__ __forceinline__ void operator()(const Acc& acc, const Unit& u, int wr, int wc, int fr, int fq, const LAS float* tab) const {
;     ...
;                     for (int bj = 0; bj < 2; ++bj) rb[ai][m][bj] = *(const u32x4*)(xb + ((size_t)u.pm * BM + ai * HALF + wr * 64 + m * 16 + fr) * D + col0 + bj * HALF);
;             asm volatile("" : "+v"(rb[0][0][0]), "+v"(rb[0][0][1]), "+v"(rb[0][1][0]), "+v"(rb[0][1][1]), "+v"(rb[0][2][0]), "+v"(rb[0][2][1]), "+v"(rb[0][3][0]), "+v"(rb[0][3][1]),
;                              "+v"(rb[1][0][0]), "+v"(rb[1][0][1]), "+v"(rb[1][1][0]), "+v"(rb[1][1][1]), "+v"(rb[1][2][0]), "+v"(rb[1][2][1]), "+v"(rb[1][3][0]), "+v"(rb[1][3][1]));
;         }
; #pragma unroll
;         for (int ai = 0; ai < 2; ++ai)
; #pragma unroll
;             for (int m = 0; m < 4; ++m) {
;                 const size_t row = (size_t)u.pm * BM + ai * HALF + wr * 64 + m * 16 + fr; const size_t off = row * D + col0; float ss = 0.f;
; #pragma unroll
;                 for (int bj = 0; bj < 2; ++bj) { f32x4 b0, b1;
;                     if (base32) { b0 = __builtin_nontemporal_load((const f32x4*)(base32 + off + bj * HALF)); b1 = __builtin_nontemporal_load((const f32x4*)(base32 + off + bj * HALF + 4)); }
;                     else { const u32x4 b4 = rb[ai][m][bj];
;                         b0 = (f32x4){__uint_as_float(b4.x << 16), __uint_as_float(b4.x & 0xFFFF0000u), __uint_as_float(b4.y << 16), __uint_as_float(b4.y & 0xFFFF0000u)};
;                         b1 = (f32x4){__uint_as_float(b4.z << 16), __uint_as_float(b4.z & 0xFFFF0000u), __uint_as_float(b4.w << 16), __uint_as_float(b4.w & 0xFFFF0000u)}; }
;                     const f32x4 o0 = b0 + acc[ai][bj][m][0], o1 = b1 + acc[ai][bj][m][1];
;                     if (out32) {
;                         if (!dry) { *(f32x4*)(out32 + off + bj * HALF) = o0; *(f32x4*)(out32 + off + bj * HALF + 4) = o1; }
.LBB0_2181:
	s_ashr_i32 s13, s12, 31
	v_lshl_or_b32 v208, s2, 8, v217
	s_lshl_b64 s[0:1], s[12:13], 8
	v_lshl_add_u64 v[210:211], s[0:1], 0, v[196:197]
	v_ashrrev_i32_e32 v209, 31, v208
	v_lshl_add_u64 v[206:207], v[208:209], 1, s[20:21]
	v_lshlrev_b64 v[66:67], 11, v[210:211]
	v_lshl_add_u64 v[212:213], v[206:207], 0, v[66:67]
	v_add_co_u32_e32 v66, vcc, 0x8000, v212
	global_load_dwordx4 v[220:223], v[212:213], off
	global_load_dwordx4 v[186:189], v[212:213], off offset:256
	v_addc_co_u32_e32 v67, vcc, 0, v213, vcc
	global_load_dwordx4 v[182:185], v[66:67], off
	global_load_dwordx4 v[178:181], v[66:67], off offset:256
	v_add_co_u32_e32 v66, vcc, 0x10000, v212
	v_cndmask_b32_e64 v214, 0, 1, s[24:25]
	s_nop 0
	v_addc_co_u32_e32 v67, vcc, 0, v213, vcc
	global_load_dwordx4 v[174:177], v[66:67], off
	global_load_dwordx4 v[170:173], v[66:67], off offset:256
	v_add_co_u32_e32 v66, vcc, 0x18000, v212
	v_cmp_ne_u32_e64 s[10:11], 1, v214
	s_nop 0
	v_addc_co_u32_e32 v67, vcc, 0, v213, vcc
	global_load_dwordx4 v[166:169], v[66:67], off
	global_load_dwordx4 v[154:157], v[66:67], off offset:256
	v_add_co_u32_e32 v66, vcc, 0x40000, v212
	v_lshlrev_b64 v[214:215], 10, v[210:211]
	s_nop 0
	v_addc_co_u32_e32 v67, vcc, 0, v213, vcc
	global_load_dwordx4 v[146:149], v[66:67], off
	global_load_dwordx4 v[138:141], v[66:67], off offset:256
	v_add_co_u32_e32 v66, vcc, 0x48000, v212
	v_lshl_add_u64 v[214:215], v[214:215], 0, v[208:209]
	s_nop 0
	v_addc_co_u32_e32 v67, vcc, 0, v213, vcc
	global_load_dwordx4 v[126:129], v[66:67], off
	global_load_dwordx4 v[114:117], v[66:67], off offset:256
	v_add_co_u32_e32 v66, vcc, 0x50000, v212
	s_mov_b64 s[12:13], -1
	s_nop 0
	v_addc_co_u32_e32 v67, vcc, 0, v213, vcc
	global_load_dwordx4 v[102:105], v[66:67], off
	global_load_dwordx4 v[90:93], v[66:67], off offset:256
	v_add_co_u32_e32 v66, vcc, 0x58000, v212
	v_lshl_add_u64 v[214:215], v[214:215], 2, s[18:19]
	s_nop 0
	v_addc_co_u32_e32 v67, vcc, 0, v213, vcc
	global_load_dwordx4 v[78:81], v[66:67], off
	s_nop 0
	global_load_dwordx4 v[66:69], v[66:67], off offset:256
	s_andn2_b64 vcc, exec, s[24:25]
	s_waitcnt vmcnt(0)
	s_nop 0
	v_lshlrev_b32_e32 v224, 16, v220
	v_and_b32_e32 v225, 0xffff0000, v220
	v_lshlrev_b32_e32 v220, 16, v221
	v_and_b32_e32 v221, 0xffff0000, v221
	v_lshlrev_b32_e32 v226, 16, v222
	v_and_b32_e32 v227, 0xffff0000, v222
	v_lshlrev_b32_e32 v222, 16, v223
	v_and_b32_e32 v223, 0xffff0000, v223
	v_pk_add_f32 v[164:165], v[164:165], v[220:221]
	v_pk_add_f32 v[162:163], v[162:163], v[224:225]
	v_pk_add_f32 v[160:161], v[160:161], v[222:223]
	v_pk_add_f32 v[158:159], v[158:159], v[226:227]
	s_cbranch_vccnz .LBB0_2183
	s_mov_b64 s[12:13], 0
	global_store_dwordx4 v[214:215], v[162:165], off sc1
	global_store_dwordx4 v[214:215], v[158:161], off offset:16 sc1

;     __device__ __forceinline__ void operator()(const Acc& acc, const Unit& u, int wr, int wc, int fr, int fq, const LAS float* tab) const {
;     ...
;                 for (int bj = 0; bj < 2; ++bj) { f32x4 b0, b1;
;                     if (base32) { b0 = __builtin_nontemporal_load((const f32x4*)(base32 + off + bj * HALF)); b1 = __builtin_nontemporal_load((const f32x4*)(base32 + off + bj * HALF + 4)); }
;                     else { const u32x4 b4 = rb[ai][m][bj];
;                         b0 = (f32x4){__uint_as_float(b4.x << 16), __uint_as_float(b4.x & 0xFFFF0000u), __uint_as_float(b4.y << 16), __uint_as_float(b4.y & 0xFFFF0000u)};
;                         b1 = (f32x4){__uint_as_float(b4.z << 16), __uint_as_float(b4.z & 0xFFFF0000u), __uint_as_float(b4.w << 16), __uint_as_float(b4.w & 0xFFFF0000u)}; }
;                     const f32x4 o0 = b0 + acc[ai][bj][m][0], o1 = b1 + acc[ai][bj][m][1];
;                     if (out32) {
;                         if (!dry) { *(f32x4*)(out32 + off + bj * HALF) = o0; *(f32x4*)(out32 + off + bj * HALF + 4) = o1; }
.LBB0_2185:
	v_lshlrev_b32_e32 v158, 16, v186
	v_and_b32_e32 v159, 0xffff0000, v186
	v_lshlrev_b32_e32 v160, 16, v187
	v_and_b32_e32 v161, 0xffff0000, v187
	v_lshlrev_b32_e32 v162, 16, v188
	v_and_b32_e32 v163, 0xffff0000, v188
	v_lshlrev_b32_e32 v164, 16, v189
	v_and_b32_e32 v165, 0xffff0000, v189
	v_pk_add_f32 v[152:153], v[152:153], v[160:161]
	v_pk_add_f32 v[150:151], v[150:151], v[158:159]
	v_pk_add_f32 v[144:145], v[144:145], v[164:165]
	v_pk_add_f32 v[142:143], v[142:143], v[162:163]
	s_and_b64 vcc, exec, s[10:11]
	s_mov_b64 s[12:13], -1
	s_cbranch_vccnz .LBB0_2187
	s_mov_b64 s[12:13], 0
	global_store_dwordx4 v[214:215], v[150:153], off offset:512 sc1
	global_store_dwordx4 v[214:215], v[142:145], off offset:528 sc1

; __device__ __forceinline__ void st16_wt(void* p, u32x4 v) { asm volatile("global_store_dwordx4 %0, %1, off sc1\n\ts_nop 1" :: "v"(p), "v"(v) : "memory"); }
; __device__ __forceinline__ unsigned cvt_pk_bf16(float lo, float hi) { unsigned r; asm volatile("v_cvt_pk_bf16_f32 %0, %1, %2" : "=v"(r) : "v"(lo), "v"(hi)); return r; }
;     __device__ __forceinline__ void operator()(const Acc& acc, const Unit& u, int wr, int wc, int fr, int fq, const LAS float* tab) const {
;     ...
;                     ss += ((o0[0] * o0[0] + o0[1] * o0[1]) + (o0[2] * o0[2] + o0[3] * o0[3])) + ((o1[0] * o1[0] + o1[1] * o1[1]) + (o1[2] * o1[2] + o1[3] * o1[3]));
;                     u32x4 w; w.x = cvt_pk_bf16(o0[0], o0[1]); w.y = cvt_pk_bf16(o0[2], o0[3]); w.z = cvt_pk_bf16(o1[0], o1[1]); w.w = cvt_pk_bf16(o1[2], o1[3]);
;                     if (!dry) st16_wt(xb + off + bj * HALF, w); }
;                 if (out32) continue;
;                 ss = sum_rows4(ss);
;                 if (fq == 0 && !dry) ssp[row * 16 + u.pn * 4 + wc] = ss;
.LBB0_2189:
	s_lshl_b32 s0, s2, 2
	s_ashr_i32 s1, s0, 31
	s_lshl_b64 s[0:1], s[0:1], 2
	s_add_u32 s34, s55, s0
	v_cndmask_b32_e64 v142, 0, 1, s[22:23]
	s_addc_u32 s35, s56, s1
	v_cmp_ne_u32_e64 s[12:13], 1, v142
	s_andn2_b64 vcc, exec, s[22:23]
	s_cbranch_vccnz .LBB0_2193
	v_mov_b32_e32 v142, v219
	s_nop 1
	v_permlane16_swap_b32_e32 v219, v142
	v_add_f32_e32 v142, v219, v142
	v_mov_b32_e32 v143, v142
	s_nop 1
	v_permlane32_swap_b32_e32 v142, v143
	s_and_saveexec_b64 s[36:37], s[6:7]
	s_cbranch_execz .LBB0_2192
	v_add_f32_e32 v144, v142, v143
	v_lshlrev_b64 v[142:143], 6, v[210:211]
	v_lshl_add_u64 v[142:143], s[34:35], 0, v[142:143]
	global_store_dword v[142:143], v144, off sc1

;     __device__ __forceinline__ void operator()(const Acc& acc, const Unit& u, int wr, int wc, int fr, int fq, const LAS float* tab) const {
;     ...
;                 const size_t row = (size_t)u.pm * BM + ai * HALF + wr * 64 + m * 16 + fr; const size_t off = row * D + col0; float ss = 0.f;
; #pragma unroll
;                 for (int bj = 0; bj < 2; ++bj) { f32x4 b0, b1;
;                     if (base32) { b0 = __builtin_nontemporal_load((const f32x4*)(base32 + off + bj * HALF)); b1 = __builtin_nontemporal_load((const f32x4*)(base32 + off + bj * HALF + 4)); }
;                     else { const u32x4 b4 = rb[ai][m][bj];
;                         b0 = (f32x4){__uint_as_float(b4.x << 16), __uint_as_float(b4.x & 0xFFFF0000u), __uint_as_float(b4.y << 16), __uint_as_float(b4.y & 0xFFFF0000u)};
;                         b1 = (f32x4){__uint_as_float(b4.z << 16), __uint_as_float(b4.z & 0xFFFF0000u), __uint_as_float(b4.w << 16), __uint_as_float(b4.w & 0xFFFF0000u)}; }
;                     const f32x4 o0 = b0 + acc[ai][bj][m][0], o1 = b1 + acc[ai][bj][m][1];
;                     if (out32) {
;                         if (!dry) { *(f32x4*)(out32 + off + bj * HALF) = o0; *(f32x4*)(out32 + off + bj * HALF + 4) = o1; }
.LBB0_2193:
	v_or_b32_e32 v142, 16, v210
	v_mov_b32_e32 v143, v211
	v_lshlrev_b64 v[144:145], 10, v[142:143]
	v_lshl_add_u64 v[144:145], v[144:145], 0, v[208:209]
	v_lshlrev_b32_e32 v150, 16, v182
	v_and_b32_e32 v151, 0xffff0000, v182
	v_lshlrev_b32_e32 v152, 16, v183
	v_and_b32_e32 v153, 0xffff0000, v183
	v_lshlrev_b32_e32 v158, 16, v184
	v_and_b32_e32 v159, 0xffff0000, v184
	v_lshlrev_b32_e32 v160, 16, v185
	v_and_b32_e32 v161, 0xffff0000, v185
	v_pk_add_f32 v[136:137], v[136:137], v[152:153]
	v_pk_add_f32 v[134:135], v[134:135], v[150:151]
	v_pk_add_f32 v[132:133], v[132:133], v[160:161]
	v_pk_add_f32 v[130:131], v[130:131], v[158:159]
	s_mov_b64 s[36:37], -1
	s_and_b64 vcc, exec, s[10:11]
	v_lshl_add_u64 v[150:151], v[144:145], 2, s[18:19]
	s_cbranch_vccnz .LBB0_2195
	s_mov_b64 s[36:37], 0
	global_store_dwordx4 v[150:151], v[134:137], off sc1
	global_store_dwordx4 v[150:151], v[130:133], off offset:16 sc1

;     __device__ __forceinline__ void operator()(const Acc& acc, const Unit& u, int wr, int wc, int fr, int fq, const LAS float* tab) const {
;     ...
;                 for (int bj = 0; bj < 2; ++bj) { f32x4 b0, b1;
;                     if (base32) { b0 = __builtin_nontemporal_load((const f32x4*)(base32 + off + bj * HALF)); b1 = __builtin_nontemporal_load((const f32x4*)(base32 + off + bj * HALF + 4)); }
;                     else { const u32x4 b4 = rb[ai][m][bj];
;                         b0 = (f32x4){__uint_as_float(b4.x << 16), __uint_as_float(b4.x & 0xFFFF0000u), __uint_as_float(b4.y << 16), __uint_as_float(b4.y & 0xFFFF0000u)};
;                         b1 = (f32x4){__uint_as_float(b4.z << 16), __uint_as_float(b4.z & 0xFFFF0000u), __uint_as_float(b4.w << 16), __uint_as_float(b4.w & 0xFFFF0000u)}; }
;                     const f32x4 o0 = b0 + acc[ai][bj][m][0], o1 = b1 + acc[ai][bj][m][1];
;                     if (out32) {
;                         if (!dry) { *(f32x4*)(out32 + off + bj * HALF) = o0; *(f32x4*)(out32 + off + bj * HALF + 4) = o1; }
.LBB0_2197:
	v_lshlrev_b32_e32 v130, 16, v178
	v_and_b32_e32 v131, 0xffff0000, v178
	v_lshlrev_b32_e32 v132, 16, v179
	v_and_b32_e32 v133, 0xffff0000, v179
	v_lshlrev_b32_e32 v134, 16, v180
	v_and_b32_e32 v135, 0xffff0000, v180
	v_lshlrev_b32_e32 v136, 16, v181
	v_and_b32_e32 v137, 0xffff0000, v181
	v_pk_add_f32 v[124:125], v[124:125], v[132:133]
	v_pk_add_f32 v[122:123], v[122:123], v[130:131]
	v_pk_add_f32 v[120:121], v[120:121], v[136:137]
	v_pk_add_f32 v[118:119], v[118:119], v[134:135]
	s_and_b64 vcc, exec, s[10:11]
	s_mov_b64 s[36:37], -1
	s_cbranch_vccnz .LBB0_2200
	global_store_dwordx4 v[150:151], v[122:125], off offset:512 sc1
	global_store_dwordx4 v[150:151], v[118:121], off offset:528 sc1
	s_cbranch_execz .LBB0_2201

; __device__ __forceinline__ void st16_wt(void* p, u32x4 v) { asm volatile("global_store_dwordx4 %0, %1, off sc1\n\ts_nop 1" :: "v"(p), "v"(v) : "memory"); }
; __device__ __forceinline__ unsigned cvt_pk_bf16(float lo, float hi) { unsigned r; asm volatile("v_cvt_pk_bf16_f32 %0, %1, %2" : "=v"(r) : "v"(lo), "v"(hi)); return r; }
;     __device__ __forceinline__ void operator()(const Acc& acc, const Unit& u, int wr, int wc, int fr, int fq, const LAS float* tab) const {
;     ...
;                     ss += ((o0[0] * o0[0] + o0[1] * o0[1]) + (o0[2] * o0[2] + o0[3] * o0[3])) + ((o1[0] * o1[0] + o1[1] * o1[1]) + (o1[2] * o1[2] + o1[3] * o1[3]));
;                     u32x4 w; w.x = cvt_pk_bf16(o0[0], o0[1]); w.y = cvt_pk_bf16(o0[2], o0[3]); w.z = cvt_pk_bf16(o1[0], o1[1]); w.w = cvt_pk_bf16(o1[2], o1[3]);
;                     if (!dry) st16_wt(xb + off + bj * HALF, w); }
;                 if (out32) continue;
;                 ss = sum_rows4(ss);
;                 if (fq == 0 && !dry) ssp[row * 16 + u.pn * 4 + wc] = ss;
.LBB0_2202:
	v_mov_b32_e32 v118, v152
	s_nop 1
	v_permlane16_swap_b32_e32 v152, v118
	v_add_f32_e32 v118, v152, v118
	v_mov_b32_e32 v119, v118
	s_nop 1
	v_permlane32_swap_b32_e32 v118, v119
	s_and_saveexec_b64 s[36:37], s[6:7]
	s_cbranch_execz .LBB0_2204
	v_add_f32_e32 v120, v118, v119
	v_lshlrev_b64 v[118:119], 6, v[142:143]
	v_lshl_add_u64 v[118:119], s[34:35], 0, v[118:119]
	global_store_dword v[118:119], v120, off sc1

;     __device__ __forceinline__ void operator()(const Acc& acc, const Unit& u, int wr, int wc, int fr, int fq, const LAS float* tab) const {
;     ...
;                 const size_t row = (size_t)u.pm * BM + ai * HALF + wr * 64 + m * 16 + fr; const size_t off = row * D + col0; float ss = 0.f;
; #pragma unroll
;                 for (int bj = 0; bj < 2; ++bj) { f32x4 b0, b1;
;                     if (base32) { b0 = __builtin_nontemporal_load((const f32x4*)(base32 + off + bj * HALF)); b1 = __builtin_nontemporal_load((const f32x4*)(base32 + off + bj * HALF + 4)); }
;                     else { const u32x4 b4 = rb[ai][m][bj];
;                         b0 = (f32x4){__uint_as_float(b4.x << 16), __uint_as_float(b4.x & 0xFFFF0000u), __uint_as_float(b4.y << 16), __uint_as_float(b4.y & 0xFFFF0000u)};
;                         b1 = (f32x4){__uint_as_float(b4.z << 16), __uint_as_float(b4.z & 0xFFFF0000u), __uint_as_float(b4.w << 16), __uint_as_float(b4.w & 0xFFFF0000u)}; }
;                     const f32x4 o0 = b0 + acc[ai][bj][m][0], o1 = b1 + acc[ai][bj][m][1];
;                     if (out32) {
;                         if (!dry) { *(f32x4*)(out32 + off + bj * HALF) = o0; *(f32x4*)(out32 + off + bj * HALF + 4) = o1; }
.LBB0_2205:
	v_or_b32_e32 v118, 32, v210
	v_mov_b32_e32 v119, v211
	v_lshlrev_b64 v[120:121], 10, v[118:119]
	v_lshl_add_u64 v[120:121], v[120:121], 0, v[208:209]
	v_lshlrev_b32_e32 v122, 16, v174
	v_and_b32_e32 v123, 0xffff0000, v174
	v_lshlrev_b32_e32 v124, 16, v175
	v_and_b32_e32 v125, 0xffff0000, v175
	v_lshlrev_b32_e32 v130, 16, v176
	v_and_b32_e32 v131, 0xffff0000, v176
	v_lshlrev_b32_e32 v132, 16, v177
	v_and_b32_e32 v133, 0xffff0000, v177
	v_pk_add_f32 v[112:113], v[112:113], v[124:125]
	v_pk_add_f32 v[110:111], v[110:111], v[122:123]
	v_pk_add_f32 v[108:109], v[108:109], v[132:133]
	v_pk_add_f32 v[106:107], v[106:107], v[130:131]
	s_mov_b64 s[36:37], -1
	s_and_b64 vcc, exec, s[10:11]
	v_lshl_add_u64 v[122:123], v[120:121], 2, s[18:19]
	s_cbranch_vccnz .LBB0_2207
	s_mov_b64 s[36:37], 0
	global_store_dwordx4 v[122:123], v[110:113], off sc1
	global_store_dwordx4 v[122:123], v[106:109], off offset:16 sc1

;     __device__ __forceinline__ void operator()(const Acc& acc, const Unit& u, int wr, int wc, int fr, int fq, const LAS float* tab) const {
;     ...
;                 for (int bj = 0; bj < 2; ++bj) { f32x4 b0, b1;
;                     if (base32) { b0 = __builtin_nontemporal_load((const f32x4*)(base32 + off + bj * HALF)); b1 = __builtin_nontemporal_load((const f32x4*)(base32 + off + bj * HALF + 4)); }
;                     else { const u32x4 b4 = rb[ai][m][bj];
;                         b0 = (f32x4){__uint_as_float(b4.x << 16), __uint_as_float(b4.x & 0xFFFF0000u), __uint_as_float(b4.y << 16), __uint_as_float(b4.y & 0xFFFF0000u)};
;                         b1 = (f32x4){__uint_as_float(b4.z << 16), __uint_as_float(b4.z & 0xFFFF0000u), __uint_as_float(b4.w << 16), __uint_as_float(b4.w & 0xFFFF0000u)}; }
;                     const f32x4 o0 = b0 + acc[ai][bj][m][0], o1 = b1 + acc[ai][bj][m][1];
;                     if (out32) {
;                         if (!dry) { *(f32x4*)(out32 + off + bj * HALF) = o0; *(f32x4*)(out32 + off + bj * HALF + 4) = o1; }
.LBB0_2209:
	v_lshlrev_b32_e32 v106, 16, v170
	v_and_b32_e32 v107, 0xffff0000, v170
	v_lshlrev_b32_e32 v108, 16, v171
	v_and_b32_e32 v109, 0xffff0000, v171
	v_lshlrev_b32_e32 v110, 16, v172
	v_and_b32_e32 v111, 0xffff0000, v172
	v_lshlrev_b32_e32 v112, 16, v173
	v_and_b32_e32 v113, 0xffff0000, v173
	v_pk_add_f32 v[100:101], v[100:101], v[108:109]
	v_pk_add_f32 v[98:99], v[98:99], v[106:107]
	v_pk_add_f32 v[96:97], v[96:97], v[112:113]
	v_pk_add_f32 v[94:95], v[94:95], v[110:111]
	s_and_b64 vcc, exec, s[10:11]
	s_mov_b64 s[36:37], -1
	s_cbranch_vccnz .LBB0_2212
	global_store_dwordx4 v[122:123], v[98:101], off offset:512 sc1
	global_store_dwordx4 v[122:123], v[94:97], off offset:528 sc1
	s_cbranch_execz .LBB0_2213

; __device__ __forceinline__ void st16_wt(void* p, u32x4 v) { asm volatile("global_store_dwordx4 %0, %1, off sc1\n\ts_nop 1" :: "v"(p), "v"(v) : "memory"); }
; __device__ __forceinline__ unsigned cvt_pk_bf16(float lo, float hi) { unsigned r; asm volatile("v_cvt_pk_bf16_f32 %0, %1, %2" : "=v"(r) : "v"(lo), "v"(hi)); return r; }
;     __device__ __forceinline__ void operator()(const Acc& acc, const Unit& u, int wr, int wc, int fr, int fq, const LAS float* tab) const {
;     ...
;                     ss += ((o0[0] * o0[0] + o0[1] * o0[1]) + (o0[2] * o0[2] + o0[3] * o0[3])) + ((o1[0] * o1[0] + o1[1] * o1[1]) + (o1[2] * o1[2] + o1[3] * o1[3]));
;                     u32x4 w; w.x = cvt_pk_bf16(o0[0], o0[1]); w.y = cvt_pk_bf16(o0[2], o0[3]); w.z = cvt_pk_bf16(o1[0], o1[1]); w.w = cvt_pk_bf16(o1[2], o1[3]);
;                     if (!dry) st16_wt(xb + off + bj * HALF, w); }
;                 if (out32) continue;
;                 ss = sum_rows4(ss);
;                 if (fq == 0 && !dry) ssp[row * 16 + u.pn * 4 + wc] = ss;
.LBB0_2214:
	v_mov_b32_e32 v94, v124
	s_nop 1
	v_permlane16_swap_b32_e32 v124, v94
	v_add_f32_e32 v94, v124, v94
	v_mov_b32_e32 v95, v94
	s_nop 1
	v_permlane32_swap_b32_e32 v94, v95
	s_and_saveexec_b64 s[36:37], s[6:7]
	s_cbranch_execz .LBB0_2216
	v_add_f32_e32 v96, v94, v95
	v_lshlrev_b64 v[94:95], 6, v[118:119]
	v_lshl_add_u64 v[94:95], s[34:35], 0, v[94:95]
	global_store_dword v[94:95], v96, off sc1

; __device__ __forceinline__ void st16_wt(void* p, u32x4 v) { asm volatile("global_store_dwordx4 %0, %1, off sc1\n\ts_nop 1" :: "v"(p), "v"(v) : "memory"); }
; __device__ __forceinline__ unsigned cvt_pk_bf16(float lo, float hi) { unsigned r; asm volatile("v_cvt_pk_bf16_f32 %0, %1, %2" : "=v"(r) : "v"(lo), "v"(hi)); return r; }
;     __device__ __forceinline__ void operator()(const Acc& acc, const Unit& u, int wr, int wc, int fr, int fq, const LAS float* tab) const {
;     ...
;                 const size_t row = (size_t)u.pm * BM + ai * HALF + wr * 64 + m * 16 + fr; const size_t off = row * D + col0; float ss = 0.f;
; #pragma unroll
;                 for (int bj = 0; bj < 2; ++bj) { f32x4 b0, b1;
;                     if (base32) { b0 = __builtin_nontemporal_load((const f32x4*)(base32 + off + bj * HALF)); b1 = __builtin_nontemporal_load((const f32x4*)(base32 + off + bj * HALF + 4)); }
;                     else { const u32x4 b4 = rb[ai][m][bj];
;                         b0 = (f32x4){__uint_as_float(b4.x << 16), __uint_as_float(b4.x & 0xFFFF0000u), __uint_as_float(b4.y << 16), __uint_as_float(b4.y & 0xFFFF0000u)};
;                         b1 = (f32x4){__uint_as_float(b4.z << 16), __uint_as_float(b4.z & 0xFFFF0000u), __uint_as_float(b4.w << 16), __uint_as_float(b4.w & 0xFFFF0000u)}; }
;                     const f32x4 o0 = b0 + acc[ai][bj][m][0], o1 = b1 + acc[ai][bj][m][1];
;                     if (out32) {
;                         if (!dry) { *(f32x4*)(out32 + off + bj * HALF) = o0; *(f32x4*)(out32 + off + bj * HALF + 4) = o1; }
;                         continue; }
;                     ss += ((o0[0] * o0[0] + o0[1] * o0[1]) + (o0[2] * o0[2] + o0[3] * o0[3])) + ((o1[0] * o1[0] + o1[1] * o1[1]) + (o1[2] * o1[2] + o1[3] * o1[3]));
;                     u32x4 w; w.x = cvt_pk_bf16(o0[0], o0[1]); w.y = cvt_pk_bf16(o0[2], o0[3]); w.z = cvt_pk_bf16(o1[0], o1[1]); w.w = cvt_pk_bf16(o1[2], o1[3]);
;                     if (!dry) st16_wt(xb + off + bj * HALF, w); }
.LBB0_2217:
	v_or_b32_e32 v94, 48, v210
	v_mov_b32_e32 v95, v211
	v_lshlrev_b64 v[96:97], 10, v[94:95]
	v_lshl_add_u64 v[96:97], v[96:97], 0, v[208:209]
	v_lshlrev_b32_e32 v98, 16, v166
	v_and_b32_e32 v99, 0xffff0000, v166
	v_lshlrev_b32_e32 v100, 16, v167
	v_and_b32_e32 v101, 0xffff0000, v167
	v_lshlrev_b32_e32 v106, 16, v168
	v_and_b32_e32 v107, 0xffff0000, v168
	v_lshlrev_b32_e32 v108, 16, v169
	v_and_b32_e32 v109, 0xffff0000, v169
	v_pk_add_f32 v[88:89], v[88:89], v[100:101]
	v_pk_add_f32 v[86:87], v[86:87], v[98:99]
	v_pk_add_f32 v[84:85], v[84:85], v[108:109]
	v_pk_add_f32 v[82:83], v[82:83], v[106:107]
	s_mov_b64 s[36:37], -1
	s_and_b64 vcc, exec, s[10:11]
	v_lshl_add_u64 v[98:99], v[96:97], 2, s[18:19]
	s_cbranch_vccnz .LBB0_2219
	s_mov_b64 s[36:37], 0
	global_store_dwordx4 v[98:99], v[86:89], off sc1
	global_store_dwordx4 v[98:99], v[82:85], off offset:16 sc1

; __device__ __forceinline__ void st16_wt(void* p, u32x4 v) { asm volatile("global_store_dwordx4 %0, %1, off sc1\n\ts_nop 1" :: "v"(p), "v"(v) : "memory"); }
; __device__ __forceinline__ unsigned cvt_pk_bf16(float lo, float hi) { unsigned r; asm volatile("v_cvt_pk_bf16_f32 %0, %1, %2" : "=v"(r) : "v"(lo), "v"(hi)); return r; }
;     __device__ __forceinline__ void operator()(const Acc& acc, const Unit& u, int wr, int wc, int fr, int fq, const LAS float* tab) const {
;     ...
;                 for (int bj = 0; bj < 2; ++bj) { f32x4 b0, b1;
;                     if (base32) { b0 = __builtin_nontemporal_load((const f32x4*)(base32 + off + bj * HALF)); b1 = __builtin_nontemporal_load((const f32x4*)(base32 + off + bj * HALF + 4)); }
;                     else { const u32x4 b4 = rb[ai][m][bj];
;                         b0 = (f32x4){__uint_as_float(b4.x << 16), __uint_as_float(b4.x & 0xFFFF0000u), __uint_as_float(b4.y << 16), __uint_as_float(b4.y & 0xFFFF0000u)};
;                         b1 = (f32x4){__uint_as_float(b4.z << 16), __uint_as_float(b4.z & 0xFFFF0000u), __uint_as_float(b4.w << 16), __uint_as_float(b4.w & 0xFFFF0000u)}; }
;                     const f32x4 o0 = b0 + acc[ai][bj][m][0], o1 = b1 + acc[ai][bj][m][1];
;                     if (out32) {
;                         if (!dry) { *(f32x4*)(out32 + off + bj * HALF) = o0; *(f32x4*)(out32 + off + bj * HALF + 4) = o1; }
;                         continue; }
;                     ss += ((o0[0] * o0[0] + o0[1] * o0[1]) + (o0[2] * o0[2] + o0[3] * o0[3])) + ((o1[0] * o1[0] + o1[1] * o1[1]) + (o1[2] * o1[2] + o1[3] * o1[3]));
;                     u32x4 w; w.x = cvt_pk_bf16(o0[0], o0[1]); w.y = cvt_pk_bf16(o0[2], o0[3]); w.z = cvt_pk_bf16(o1[0], o1[1]); w.w = cvt_pk_bf16(o1[2], o1[3]);
;                     if (!dry) st16_wt(xb + off + bj * HALF, w); }
.LBB0_2221:
	v_lshlrev_b32_e32 v82, 16, v154
	v_and_b32_e32 v83, 0xffff0000, v154
	v_lshlrev_b32_e32 v84, 16, v155
	v_and_b32_e32 v85, 0xffff0000, v155
	v_lshlrev_b32_e32 v86, 16, v156
	v_and_b32_e32 v87, 0xffff0000, v156
	v_lshlrev_b32_e32 v88, 16, v157
	v_and_b32_e32 v89, 0xffff0000, v157
	v_pk_add_f32 v[76:77], v[76:77], v[84:85]
	v_pk_add_f32 v[74:75], v[74:75], v[82:83]
	v_pk_add_f32 v[72:73], v[72:73], v[88:89]
	v_pk_add_f32 v[70:71], v[70:71], v[86:87]
	s_and_b64 vcc, exec, s[10:11]
	s_mov_b64 s[36:37], -1
	s_cbranch_vccnz .LBB0_2224
	global_store_dwordx4 v[98:99], v[74:77], off offset:512 sc1
	global_store_dwordx4 v[98:99], v[70:73], off offset:528 sc1
	s_cbranch_execz .LBB0_2225

; __device__ __forceinline__ void st16_wt(void* p, u32x4 v) { asm volatile("global_store_dwordx4 %0, %1, off sc1\n\ts_nop 1" :: "v"(p), "v"(v) : "memory"); }
; __device__ __forceinline__ unsigned cvt_pk_bf16(float lo, float hi) { unsigned r; asm volatile("v_cvt_pk_bf16_f32 %0, %1, %2" : "=v"(r) : "v"(lo), "v"(hi)); return r; }
; __device__ __forceinline__ float sum_rows4(float v) {
;     const auto a = __builtin_amdgcn_permlane16_swap(__float_as_uint(v), __float_as_uint(v), false, false); const float s = __uint_as_float(a[0]) + __uint_as_float(a[1]);
;     const auto b = __builtin_amdgcn_permlane32_swap(__float_as_uint(s), __float_as_uint(s), false, false); return __uint_as_float(b[0]) + __uint_as_float(b[1]);
;     __device__ __forceinline__ void operator()(const Acc& acc, const Unit& u, int wr, int wc, int fr, int fq, const LAS float* tab) const {
;     ...
;                     ss += ((o0[0] * o0[0] + o0[1] * o0[1]) + (o0[2] * o0[2] + o0[3] * o0[3])) + ((o1[0] * o1[0] + o1[1] * o1[1]) + (o1[2] * o1[2] + o1[3] * o1[3]));
;                     u32x4 w; w.x = cvt_pk_bf16(o0[0], o0[1]); w.y = cvt_pk_bf16(o0[2], o0[3]); w.z = cvt_pk_bf16(o1[0], o1[1]); w.w = cvt_pk_bf16(o1[2], o1[3]);
;                     if (!dry) st16_wt(xb + off + bj * HALF, w); }
;                 if (out32) continue;
;                 ss = sum_rows4(ss);
;                 if (fq == 0 && !dry) ssp[row * 16 + u.pn * 4 + wc] = ss;
.LBB0_2226:
	v_mov_b32_e32 v70, v100
	s_nop 1
	v_permlane16_swap_b32_e32 v100, v70
	v_add_f32_e32 v70, v100, v70
	v_mov_b32_e32 v71, v70
	s_nop 1
	v_permlane32_swap_b32_e32 v70, v71
	s_and_saveexec_b64 s[36:37], s[6:7]
	s_cbranch_execz .LBB0_2228
	v_add_f32_e32 v72, v70, v71
	v_lshlrev_b64 v[70:71], 6, v[94:95]
	v_lshl_add_u64 v[70:71], s[34:35], 0, v[70:71]
	global_store_dword v[70:71], v72, off sc1

; __device__ __forceinline__ void st16_wt(void* p, u32x4 v) { asm volatile("global_store_dwordx4 %0, %1, off sc1\n\ts_nop 1" :: "v"(p), "v"(v) : "memory"); }
; __device__ __forceinline__ unsigned cvt_pk_bf16(float lo, float hi) { unsigned r; asm volatile("v_cvt_pk_bf16_f32 %0, %1, %2" : "=v"(r) : "v"(lo), "v"(hi)); return r; }
;     __device__ __forceinline__ void operator()(const Acc& acc, const Unit& u, int wr, int wc, int fr, int fq, const LAS float* tab) const {
;     ...
;                 const size_t row = (size_t)u.pm * BM + ai * HALF + wr * 64 + m * 16 + fr; const size_t off = row * D + col0; float ss = 0.f;
; #pragma unroll
;                 for (int bj = 0; bj < 2; ++bj) { f32x4 b0, b1;
;                     if (base32) { b0 = __builtin_nontemporal_load((const f32x4*)(base32 + off + bj * HALF)); b1 = __builtin_nontemporal_load((const f32x4*)(base32 + off + bj * HALF + 4)); }
;                     else { const u32x4 b4 = rb[ai][m][bj];
;                         b0 = (f32x4){__uint_as_float(b4.x << 16), __uint_as_float(b4.x & 0xFFFF0000u), __uint_as_float(b4.y << 16), __uint_as_float(b4.y & 0xFFFF0000u)};
;                         b1 = (f32x4){__uint_as_float(b4.z << 16), __uint_as_float(b4.z & 0xFFFF0000u), __uint_as_float(b4.w << 16), __uint_as_float(b4.w & 0xFFFF0000u)}; }
;                     const f32x4 o0 = b0 + acc[ai][bj][m][0], o1 = b1 + acc[ai][bj][m][1];
;                     if (out32) {
;                         if (!dry) { *(f32x4*)(out32 + off + bj * HALF) = o0; *(f32x4*)(out32 + off + bj * HALF + 4) = o1; }
;                         continue; }
;                     ss += ((o0[0] * o0[0] + o0[1] * o0[1]) + (o0[2] * o0[2] + o0[3] * o0[3])) + ((o1[0] * o1[0] + o1[1] * o1[1]) + (o1[2] * o1[2] + o1[3] * o1[3]));
;                     u32x4 w; w.x = cvt_pk_bf16(o0[0], o0[1]); w.y = cvt_pk_bf16(o0[2], o0[3]); w.z = cvt_pk_bf16(o1[0], o1[1]); w.w = cvt_pk_bf16(o1[2], o1[3]);
;                     if (!dry) st16_wt(xb + off + bj * HALF, w); }
.LBB0_2229:
	v_lshl_add_u64 v[70:71], v[210:211], 0, s[90:91]
	v_lshlrev_b64 v[72:73], 10, v[70:71]
	v_lshl_add_u64 v[72:73], v[72:73], 0, v[208:209]
	v_lshlrev_b32_e32 v74, 16, v146
	v_and_b32_e32 v75, 0xffff0000, v146
	v_lshlrev_b32_e32 v76, 16, v147
	v_and_b32_e32 v77, 0xffff0000, v147
	v_lshlrev_b32_e32 v82, 16, v148
	v_and_b32_e32 v83, 0xffff0000, v148
	v_lshlrev_b32_e32 v84, 16, v149
	v_and_b32_e32 v85, 0xffff0000, v149
	v_pk_add_f32 v[64:65], v[64:65], v[76:77]
	v_pk_add_f32 v[62:63], v[62:63], v[74:75]
	v_pk_add_f32 v[60:61], v[60:61], v[84:85]
	v_pk_add_f32 v[58:59], v[58:59], v[82:83]
	s_mov_b64 s[36:37], -1
	s_and_b64 vcc, exec, s[10:11]
	v_lshl_add_u64 v[74:75], v[72:73], 2, s[18:19]
	s_cbranch_vccnz .LBB0_2231
	s_mov_b64 s[36:37], 0
	global_store_dwordx4 v[74:75], v[62:65], off sc1
	global_store_dwordx4 v[74:75], v[58:61], off offset:16 sc1

; __device__ __forceinline__ void st16_wt(void* p, u32x4 v) { asm volatile("global_store_dwordx4 %0, %1, off sc1\n\ts_nop 1" :: "v"(p), "v"(v) : "memory"); }
; __device__ __forceinline__ unsigned cvt_pk_bf16(float lo, float hi) { unsigned r; asm volatile("v_cvt_pk_bf16_f32 %0, %1, %2" : "=v"(r) : "v"(lo), "v"(hi)); return r; }
;     __device__ __forceinline__ void operator()(const Acc& acc, const Unit& u, int wr, int wc, int fr, int fq, const LAS float* tab) const {
;     ...
;                 for (int bj = 0; bj < 2; ++bj) { f32x4 b0, b1;
;                     if (base32) { b0 = __builtin_nontemporal_load((const f32x4*)(base32 + off + bj * HALF)); b1 = __builtin_nontemporal_load((const f32x4*)(base32 + off + bj * HALF + 4)); }
;                     else { const u32x4 b4 = rb[ai][m][bj];
;                         b0 = (f32x4){__uint_as_float(b4.x << 16), __uint_as_float(b4.x & 0xFFFF0000u), __uint_as_float(b4.y << 16), __uint_as_float(b4.y & 0xFFFF0000u)};
;                         b1 = (f32x4){__uint_as_float(b4.z << 16), __uint_as_float(b4.z & 0xFFFF0000u), __uint_as_float(b4.w << 16), __uint_as_float(b4.w & 0xFFFF0000u)}; }
;                     const f32x4 o0 = b0 + acc[ai][bj][m][0], o1 = b1 + acc[ai][bj][m][1];
;                     if (out32) {
;                         if (!dry) { *(f32x4*)(out32 + off + bj * HALF) = o0; *(f32x4*)(out32 + off + bj * HALF + 4) = o1; }
;                         continue; }
;                     ss += ((o0[0] * o0[0] + o0[1] * o0[1]) + (o0[2] * o0[2] + o0[3] * o0[3])) + ((o1[0] * o1[0] + o1[1] * o1[1]) + (o1[2] * o1[2] + o1[3] * o1[3]));
;                     u32x4 w; w.x = cvt_pk_bf16(o0[0], o0[1]); w.y = cvt_pk_bf16(o0[2], o0[3]); w.z = cvt_pk_bf16(o1[0], o1[1]); w.w = cvt_pk_bf16(o1[2], o1[3]);
;                     if (!dry) st16_wt(xb + off + bj * HALF, w); }
.LBB0_2233:
	v_lshlrev_b32_e32 v58, 16, v138
	v_and_b32_e32 v59, 0xffff0000, v138
	v_lshlrev_b32_e32 v60, 16, v139
	v_and_b32_e32 v61, 0xffff0000, v139
	v_lshlrev_b32_e32 v62, 16, v140
	v_and_b32_e32 v63, 0xffff0000, v140
	v_lshlrev_b32_e32 v64, 16, v141
	v_and_b32_e32 v65, 0xffff0000, v141
	v_pk_add_f32 v[56:57], v[56:57], v[60:61]
	v_pk_add_f32 v[54:55], v[54:55], v[58:59]
	v_pk_add_f32 v[52:53], v[52:53], v[64:65]
	v_pk_add_f32 v[50:51], v[50:51], v[62:63]
	s_and_b64 vcc, exec, s[10:11]
	s_mov_b64 s[36:37], -1
	s_cbranch_vccnz .LBB0_2236
	global_store_dwordx4 v[74:75], v[54:57], off offset:512 sc1
	global_store_dwordx4 v[74:75], v[50:53], off offset:528 sc1
	s_cbranch_execz .LBB0_2237

; __device__ __forceinline__ void st16_wt(void* p, u32x4 v) { asm volatile("global_store_dwordx4 %0, %1, off sc1\n\ts_nop 1" :: "v"(p), "v"(v) : "memory"); }
; __device__ __forceinline__ unsigned cvt_pk_bf16(float lo, float hi) { unsigned r; asm volatile("v_cvt_pk_bf16_f32 %0, %1, %2" : "=v"(r) : "v"(lo), "v"(hi)); return r; }
; __device__ __forceinline__ float sum_rows4(float v) {
;     const auto a = __builtin_amdgcn_permlane16_swap(__float_as_uint(v), __float_as_uint(v), false, false); const float s = __uint_as_float(a[0]) + __uint_as_float(a[1]);
;     const auto b = __builtin_amdgcn_permlane32_swap(__float_as_uint(s), __float_as_uint(s), false, false); return __uint_as_float(b[0]) + __uint_as_float(b[1]);
;     __device__ __forceinline__ void operator()(const Acc& acc, const Unit& u, int wr, int wc, int fr, int fq, const LAS float* tab) const {
;     ...
;                     ss += ((o0[0] * o0[0] + o0[1] * o0[1]) + (o0[2] * o0[2] + o0[3] * o0[3])) + ((o1[0] * o1[0] + o1[1] * o1[1]) + (o1[2] * o1[2] + o1[3] * o1[3]));
;                     u32x4 w; w.x = cvt_pk_bf16(o0[0], o0[1]); w.y = cvt_pk_bf16(o0[2], o0[3]); w.z = cvt_pk_bf16(o1[0], o1[1]); w.w = cvt_pk_bf16(o1[2], o1[3]);
;                     if (!dry) st16_wt(xb + off + bj * HALF, w); }
;                 if (out32) continue;
;                 ss = sum_rows4(ss);
;                 if (fq == 0 && !dry) ssp[row * 16 + u.pn * 4 + wc] = ss;
.LBB0_2238:
	v_mov_b32_e32 v50, v76
	s_nop 1
	v_permlane16_swap_b32_e32 v76, v50
	v_add_f32_e32 v50, v76, v50
	v_mov_b32_e32 v51, v50
	s_nop 1
	v_permlane32_swap_b32_e32 v50, v51
	s_and_saveexec_b64 s[36:37], s[6:7]
	s_cbranch_execz .LBB0_2240
	v_add_f32_e32 v52, v50, v51
	v_lshlrev_b64 v[50:51], 6, v[70:71]
	v_lshl_add_u64 v[50:51], s[34:35], 0, v[50:51]
	global_store_dword v[50:51], v52, off sc1

; __device__ __forceinline__ void st16_wt(void* p, u32x4 v) { asm volatile("global_store_dwordx4 %0, %1, off sc1\n\ts_nop 1" :: "v"(p), "v"(v) : "memory"); }
; __device__ __forceinline__ unsigned cvt_pk_bf16(float lo, float hi) { unsigned r; asm volatile("v_cvt_pk_bf16_f32 %0, %1, %2" : "=v"(r) : "v"(lo), "v"(hi)); return r; }
;     __device__ __forceinline__ void operator()(const Acc& acc, const Unit& u, int wr, int wc, int fr, int fq, const LAS float* tab) const {
;     ...
;                 const size_t row = (size_t)u.pm * BM + ai * HALF + wr * 64 + m * 16 + fr; const size_t off = row * D + col0; float ss = 0.f;
; #pragma unroll
;                 for (int bj = 0; bj < 2; ++bj) { f32x4 b0, b1;
;                     if (base32) { b0 = __builtin_nontemporal_load((const f32x4*)(base32 + off + bj * HALF)); b1 = __builtin_nontemporal_load((const f32x4*)(base32 + off + bj * HALF + 4)); }
;                     else { const u32x4 b4 = rb[ai][m][bj];
;                         b0 = (f32x4){__uint_as_float(b4.x << 16), __uint_as_float(b4.x & 0xFFFF0000u), __uint_as_float(b4.y << 16), __uint_as_float(b4.y & 0xFFFF0000u)};
;                         b1 = (f32x4){__uint_as_float(b4.z << 16), __uint_as_float(b4.z & 0xFFFF0000u), __uint_as_float(b4.w << 16), __uint_as_float(b4.w & 0xFFFF0000u)}; }
;                     const f32x4 o0 = b0 + acc[ai][bj][m][0], o1 = b1 + acc[ai][bj][m][1];
;                     if (out32) {
;                         if (!dry) { *(f32x4*)(out32 + off + bj * HALF) = o0; *(f32x4*)(out32 + off + bj * HALF + 4) = o1; }
;                         continue; }
;                     ss += ((o0[0] * o0[0] + o0[1] * o0[1]) + (o0[2] * o0[2] + o0[3] * o0[3])) + ((o1[0] * o1[0] + o1[1] * o1[1]) + (o1[2] * o1[2] + o1[3] * o1[3]));
;                     u32x4 w; w.x = cvt_pk_bf16(o0[0], o0[1]); w.y = cvt_pk_bf16(o0[2], o0[3]); w.z = cvt_pk_bf16(o1[0], o1[1]); w.w = cvt_pk_bf16(o1[2], o1[3]);
;                     if (!dry) st16_wt(xb + off + bj * HALF, w); }
.LBB0_2241:
	s_mov_b64 s[0:1], 0x90
	v_lshl_add_u64 v[50:51], v[210:211], 0, s[0:1]
	v_lshlrev_b64 v[52:53], 10, v[50:51]
	v_lshl_add_u64 v[52:53], v[52:53], 0, v[208:209]
	v_lshlrev_b32_e32 v54, 16, v126
	v_and_b32_e32 v55, 0xffff0000, v126
	v_lshlrev_b32_e32 v56, 16, v127
	v_and_b32_e32 v57, 0xffff0000, v127
	v_lshlrev_b32_e32 v58, 16, v128
	v_and_b32_e32 v59, 0xffff0000, v128
	v_lshlrev_b32_e32 v60, 16, v129
	v_and_b32_e32 v61, 0xffff0000, v129
	v_pk_add_f32 v[48:49], v[48:49], v[56:57]
	v_pk_add_f32 v[46:47], v[46:47], v[54:55]
	v_pk_add_f32 v[44:45], v[44:45], v[60:61]
	v_pk_add_f32 v[42:43], v[42:43], v[58:59]
	s_mov_b64 s[36:37], -1
	s_and_b64 vcc, exec, s[10:11]
	v_lshl_add_u64 v[54:55], v[52:53], 2, s[18:19]
	s_cbranch_vccnz .LBB0_2243
	s_mov_b64 s[36:37], 0
	global_store_dwordx4 v[54:55], v[46:49], off sc1
	global_store_dwordx4 v[54:55], v[42:45], off offset:16 sc1

; __device__ __forceinline__ void st16_wt(void* p, u32x4 v) { asm volatile("global_store_dwordx4 %0, %1, off sc1\n\ts_nop 1" :: "v"(p), "v"(v) : "memory"); }
; __device__ __forceinline__ unsigned cvt_pk_bf16(float lo, float hi) { unsigned r; asm volatile("v_cvt_pk_bf16_f32 %0, %1, %2" : "=v"(r) : "v"(lo), "v"(hi)); return r; }
;     __device__ __forceinline__ void operator()(const Acc& acc, const Unit& u, int wr, int wc, int fr, int fq, const LAS float* tab) const {
;     ...
;                 for (int bj = 0; bj < 2; ++bj) { f32x4 b0, b1;
;                     if (base32) { b0 = __builtin_nontemporal_load((const f32x4*)(base32 + off + bj * HALF)); b1 = __builtin_nontemporal_load((const f32x4*)(base32 + off + bj * HALF + 4)); }
;                     else { const u32x4 b4 = rb[ai][m][bj];
;                         b0 = (f32x4){__uint_as_float(b4.x << 16), __uint_as_float(b4.x & 0xFFFF0000u), __uint_as_float(b4.y << 16), __uint_as_float(b4.y & 0xFFFF0000u)};
;                         b1 = (f32x4){__uint_as_float(b4.z << 16), __uint_as_float(b4.z & 0xFFFF0000u), __uint_as_float(b4.w << 16), __uint_as_float(b4.w & 0xFFFF0000u)}; }
;                     const f32x4 o0 = b0 + acc[ai][bj][m][0], o1 = b1 + acc[ai][bj][m][1];
;                     if (out32) {
;                         if (!dry) { *(f32x4*)(out32 + off + bj * HALF) = o0; *(f32x4*)(out32 + off + bj * HALF + 4) = o1; }
;                         continue; }
;                     ss += ((o0[0] * o0[0] + o0[1] * o0[1]) + (o0[2] * o0[2] + o0[3] * o0[3])) + ((o1[0] * o1[0] + o1[1] * o1[1]) + (o1[2] * o1[2] + o1[3] * o1[3]));
;                     u32x4 w; w.x = cvt_pk_bf16(o0[0], o0[1]); w.y = cvt_pk_bf16(o0[2], o0[3]); w.z = cvt_pk_bf16(o1[0], o1[1]); w.w = cvt_pk_bf16(o1[2], o1[3]);
;                     if (!dry) st16_wt(xb + off + bj * HALF, w); }
.LBB0_2245:
	v_lshlrev_b32_e32 v42, 16, v114
	v_and_b32_e32 v43, 0xffff0000, v114
	v_lshlrev_b32_e32 v44, 16, v115
	v_and_b32_e32 v45, 0xffff0000, v115
	v_lshlrev_b32_e32 v46, 16, v116
	v_and_b32_e32 v47, 0xffff0000, v116
	v_lshlrev_b32_e32 v48, 16, v117
	v_and_b32_e32 v49, 0xffff0000, v117
	v_pk_add_f32 v[40:41], v[40:41], v[44:45]
	v_pk_add_f32 v[38:39], v[38:39], v[42:43]
	v_pk_add_f32 v[36:37], v[36:37], v[48:49]
	v_pk_add_f32 v[34:35], v[34:35], v[46:47]
	s_and_b64 vcc, exec, s[10:11]
	s_mov_b64 s[36:37], -1
	s_cbranch_vccnz .LBB0_2248
	global_store_dwordx4 v[54:55], v[38:41], off offset:512 sc1
	global_store_dwordx4 v[54:55], v[34:37], off offset:528 sc1
	s_cbranch_execz .LBB0_2249

; __device__ __forceinline__ void st16_wt(void* p, u32x4 v) { asm volatile("global_store_dwordx4 %0, %1, off sc1\n\ts_nop 1" :: "v"(p), "v"(v) : "memory"); }
; __device__ __forceinline__ unsigned cvt_pk_bf16(float lo, float hi) { unsigned r; asm volatile("v_cvt_pk_bf16_f32 %0, %1, %2" : "=v"(r) : "v"(lo), "v"(hi)); return r; }
; __device__ __forceinline__ float sum_rows4(float v) {
;     const auto a = __builtin_amdgcn_permlane16_swap(__float_as_uint(v), __float_as_uint(v), false, false); const float s = __uint_as_float(a[0]) + __uint_as_float(a[1]);
;     const auto b = __builtin_amdgcn_permlane32_swap(__float_as_uint(s), __float_as_uint(s), false, false); return __uint_as_float(b[0]) + __uint_as_float(b[1]);
;     __device__ __forceinline__ void operator()(const Acc& acc, const Unit& u, int wr, int wc, int fr, int fq, const LAS float* tab) const {
;     ...
;                     ss += ((o0[0] * o0[0] + o0[1] * o0[1]) + (o0[2] * o0[2] + o0[3] * o0[3])) + ((o1[0] * o1[0] + o1[1] * o1[1]) + (o1[2] * o1[2] + o1[3] * o1[3]));
;                     u32x4 w; w.x = cvt_pk_bf16(o0[0], o0[1]); w.y = cvt_pk_bf16(o0[2], o0[3]); w.z = cvt_pk_bf16(o1[0], o1[1]); w.w = cvt_pk_bf16(o1[2], o1[3]);
;                     if (!dry) st16_wt(xb + off + bj * HALF, w); }
;                 if (out32) continue;
;                 ss = sum_rows4(ss);
;                 if (fq == 0 && !dry) ssp[row * 16 + u.pn * 4 + wc] = ss;
.LBB0_2250:
	v_mov_b32_e32 v34, v56
	s_nop 1
	v_permlane16_swap_b32_e32 v56, v34
	v_add_f32_e32 v34, v56, v34
	v_mov_b32_e32 v35, v34
	s_nop 1
	v_permlane32_swap_b32_e32 v34, v35
	s_and_saveexec_b64 s[36:37], s[6:7]
	s_cbranch_execz .LBB0_2252
	v_add_f32_e32 v36, v34, v35
	v_lshlrev_b64 v[34:35], 6, v[50:51]
	v_lshl_add_u64 v[34:35], s[34:35], 0, v[34:35]
	global_store_dword v[34:35], v36, off sc1

; __device__ __forceinline__ void st16_wt(void* p, u32x4 v) { asm volatile("global_store_dwordx4 %0, %1, off sc1\n\ts_nop 1" :: "v"(p), "v"(v) : "memory"); }
; __device__ __forceinline__ unsigned cvt_pk_bf16(float lo, float hi) { unsigned r; asm volatile("v_cvt_pk_bf16_f32 %0, %1, %2" : "=v"(r) : "v"(lo), "v"(hi)); return r; }
;     __device__ __forceinline__ void operator()(const Acc& acc, const Unit& u, int wr, int wc, int fr, int fq, const LAS float* tab) const {
;     ...
;                 const size_t row = (size_t)u.pm * BM + ai * HALF + wr * 64 + m * 16 + fr; const size_t off = row * D + col0; float ss = 0.f;
; #pragma unroll
;                 for (int bj = 0; bj < 2; ++bj) { f32x4 b0, b1;
;                     if (base32) { b0 = __builtin_nontemporal_load((const f32x4*)(base32 + off + bj * HALF)); b1 = __builtin_nontemporal_load((const f32x4*)(base32 + off + bj * HALF + 4)); }
;                     else { const u32x4 b4 = rb[ai][m][bj];
;                         b0 = (f32x4){__uint_as_float(b4.x << 16), __uint_as_float(b4.x & 0xFFFF0000u), __uint_as_float(b4.y << 16), __uint_as_float(b4.y & 0xFFFF0000u)};
;                         b1 = (f32x4){__uint_as_float(b4.z << 16), __uint_as_float(b4.z & 0xFFFF0000u), __uint_as_float(b4.w << 16), __uint_as_float(b4.w & 0xFFFF0000u)}; }
;                     const f32x4 o0 = b0 + acc[ai][bj][m][0], o1 = b1 + acc[ai][bj][m][1];
;                     if (out32) {
;                         if (!dry) { *(f32x4*)(out32 + off + bj * HALF) = o0; *(f32x4*)(out32 + off + bj * HALF + 4) = o1; }
;                         continue; }
;                     ss += ((o0[0] * o0[0] + o0[1] * o0[1]) + (o0[2] * o0[2] + o0[3] * o0[3])) + ((o1[0] * o1[0] + o1[1] * o1[1]) + (o1[2] * o1[2] + o1[3] * o1[3]));
;                     u32x4 w; w.x = cvt_pk_bf16(o0[0], o0[1]); w.y = cvt_pk_bf16(o0[2], o0[3]); w.z = cvt_pk_bf16(o1[0], o1[1]); w.w = cvt_pk_bf16(o1[2], o1[3]);
;                     if (!dry) st16_wt(xb + off + bj * HALF, w); }
.LBB0_2253:
	s_mov_b64 s[0:1], 0xa0
	v_lshl_add_u64 v[34:35], v[210:211], 0, s[0:1]
	v_lshlrev_b64 v[36:37], 10, v[34:35]
	v_lshl_add_u64 v[36:37], v[36:37], 0, v[208:209]
	v_lshlrev_b32_e32 v38, 16, v102
	v_and_b32_e32 v39, 0xffff0000, v102
	v_lshlrev_b32_e32 v40, 16, v103
	v_and_b32_e32 v41, 0xffff0000, v103
	v_lshlrev_b32_e32 v42, 16, v104
	v_and_b32_e32 v43, 0xffff0000, v104
	v_lshlrev_b32_e32 v44, 16, v105
	v_and_b32_e32 v45, 0xffff0000, v105
	v_pk_add_f32 v[32:33], v[32:33], v[40:41]
	v_pk_add_f32 v[30:31], v[30:31], v[38:39]
	v_pk_add_f32 v[28:29], v[28:29], v[44:45]
	v_pk_add_f32 v[26:27], v[26:27], v[42:43]
	s_mov_b64 s[36:37], -1
	s_and_b64 vcc, exec, s[10:11]
	v_lshl_add_u64 v[38:39], v[36:37], 2, s[18:19]
	s_cbranch_vccnz .LBB0_2255
	s_mov_b64 s[36:37], 0
	global_store_dwordx4 v[38:39], v[30:33], off sc1
	global_store_dwordx4 v[38:39], v[26:29], off offset:16 sc1

; __device__ __forceinline__ void st16_wt(void* p, u32x4 v) { asm volatile("global_store_dwordx4 %0, %1, off sc1\n\ts_nop 1" :: "v"(p), "v"(v) : "memory"); }
; __device__ __forceinline__ unsigned cvt_pk_bf16(float lo, float hi) { unsigned r; asm volatile("v_cvt_pk_bf16_f32 %0, %1, %2" : "=v"(r) : "v"(lo), "v"(hi)); return r; }
;     __device__ __forceinline__ void operator()(const Acc& acc, const Unit& u, int wr, int wc, int fr, int fq, const LAS float* tab) const {
;     ...
;                 for (int bj = 0; bj < 2; ++bj) { f32x4 b0, b1;
;                     if (base32) { b0 = __builtin_nontemporal_load((const f32x4*)(base32 + off + bj * HALF)); b1 = __builtin_nontemporal_load((const f32x4*)(base32 + off + bj * HALF + 4)); }
;                     else { const u32x4 b4 = rb[ai][m][bj];
;                         b0 = (f32x4){__uint_as_float(b4.x << 16), __uint_as_float(b4.x & 0xFFFF0000u), __uint_as_float(b4.y << 16), __uint_as_float(b4.y & 0xFFFF0000u)};
;                         b1 = (f32x4){__uint_as_float(b4.z << 16), __uint_as_float(b4.z & 0xFFFF0000u), __uint_as_float(b4.w << 16), __uint_as_float(b4.w & 0xFFFF0000u)}; }
;                     const f32x4 o0 = b0 + acc[ai][bj][m][0], o1 = b1 + acc[ai][bj][m][1];
;                     if (out32) {
;                         if (!dry) { *(f32x4*)(out32 + off + bj * HALF) = o0; *(f32x4*)(out32 + off + bj * HALF + 4) = o1; }
;                         continue; }
;                     ss += ((o0[0] * o0[0] + o0[1] * o0[1]) + (o0[2] * o0[2] + o0[3] * o0[3])) + ((o1[0] * o1[0] + o1[1] * o1[1]) + (o1[2] * o1[2] + o1[3] * o1[3]));
;                     u32x4 w; w.x = cvt_pk_bf16(o0[0], o0[1]); w.y = cvt_pk_bf16(o0[2], o0[3]); w.z = cvt_pk_bf16(o1[0], o1[1]); w.w = cvt_pk_bf16(o1[2], o1[3]);
;                     if (!dry) st16_wt(xb + off + bj * HALF, w); }
.LBB0_2257:
	v_lshlrev_b32_e32 v26, 16, v90
	v_and_b32_e32 v27, 0xffff0000, v90
	v_lshlrev_b32_e32 v28, 16, v91
	v_and_b32_e32 v29, 0xffff0000, v91
	v_lshlrev_b32_e32 v30, 16, v92
	v_and_b32_e32 v31, 0xffff0000, v92
	v_lshlrev_b32_e32 v32, 16, v93
	v_and_b32_e32 v33, 0xffff0000, v93
	v_pk_add_f32 v[24:25], v[24:25], v[28:29]
	v_pk_add_f32 v[22:23], v[22:23], v[26:27]
	v_pk_add_f32 v[20:21], v[20:21], v[32:33]
	v_pk_add_f32 v[18:19], v[18:19], v[30:31]
	s_and_b64 vcc, exec, s[10:11]
	s_mov_b64 s[36:37], -1
	s_cbranch_vccnz .LBB0_2260
	global_store_dwordx4 v[38:39], v[22:25], off offset:512 sc1
	global_store_dwordx4 v[38:39], v[18:21], off offset:528 sc1
	s_cbranch_execz .LBB0_2261

; __device__ __forceinline__ void st16_wt(void* p, u32x4 v) { asm volatile("global_store_dwordx4 %0, %1, off sc1\n\ts_nop 1" :: "v"(p), "v"(v) : "memory"); }
; __device__ __forceinline__ unsigned cvt_pk_bf16(float lo, float hi) { unsigned r; asm volatile("v_cvt_pk_bf16_f32 %0, %1, %2" : "=v"(r) : "v"(lo), "v"(hi)); return r; }
; __device__ __forceinline__ float sum_rows4(float v) {
;     const auto a = __builtin_amdgcn_permlane16_swap(__float_as_uint(v), __float_as_uint(v), false, false); const float s = __uint_as_float(a[0]) + __uint_as_float(a[1]);
;     const auto b = __builtin_amdgcn_permlane32_swap(__float_as_uint(s), __float_as_uint(s), false, false); return __uint_as_float(b[0]) + __uint_as_float(b[1]);
;     __device__ __forceinline__ void operator()(const Acc& acc, const Unit& u, int wr, int wc, int fr, int fq, const LAS float* tab) const {
;     ...
;                     ss += ((o0[0] * o0[0] + o0[1] * o0[1]) + (o0[2] * o0[2] + o0[3] * o0[3])) + ((o1[0] * o1[0] + o1[1] * o1[1]) + (o1[2] * o1[2] + o1[3] * o1[3]));
;                     u32x4 w; w.x = cvt_pk_bf16(o0[0], o0[1]); w.y = cvt_pk_bf16(o0[2], o0[3]); w.z = cvt_pk_bf16(o1[0], o1[1]); w.w = cvt_pk_bf16(o1[2], o1[3]);
;                     if (!dry) st16_wt(xb + off + bj * HALF, w); }
;                 if (out32) continue;
;                 ss = sum_rows4(ss);
;                 if (fq == 0 && !dry) ssp[row * 16 + u.pn * 4 + wc] = ss;
.LBB0_2262:
	v_mov_b32_e32 v18, v40
	s_nop 1
	v_permlane16_swap_b32_e32 v40, v18
	v_add_f32_e32 v18, v40, v18
	v_mov_b32_e32 v19, v18
	s_nop 1
	v_permlane32_swap_b32_e32 v18, v19
	s_and_saveexec_b64 s[36:37], s[6:7]
	s_cbranch_execz .LBB0_2264
	v_add_f32_e32 v20, v18, v19
	v_lshlrev_b64 v[18:19], 6, v[34:35]
	v_lshl_add_u64 v[18:19], s[34:35], 0, v[18:19]
	global_store_dword v[18:19], v20, off sc1

; __device__ __forceinline__ void st16_wt(void* p, u32x4 v) { asm volatile("global_store_dwordx4 %0, %1, off sc1\n\ts_nop 1" :: "v"(p), "v"(v) : "memory"); }
; __device__ __forceinline__ unsigned cvt_pk_bf16(float lo, float hi) { unsigned r; asm volatile("v_cvt_pk_bf16_f32 %0, %1, %2" : "=v"(r) : "v"(lo), "v"(hi)); return r; }
;     __device__ __forceinline__ void operator()(const Acc& acc, const Unit& u, int wr, int wc, int fr, int fq, const LAS float* tab) const {
;     ...
;                 const size_t row = (size_t)u.pm * BM + ai * HALF + wr * 64 + m * 16 + fr; const size_t off = row * D + col0; float ss = 0.f;
; #pragma unroll
;                 for (int bj = 0; bj < 2; ++bj) { f32x4 b0, b1;
;                     if (base32) { b0 = __builtin_nontemporal_load((const f32x4*)(base32 + off + bj * HALF)); b1 = __builtin_nontemporal_load((const f32x4*)(base32 + off + bj * HALF + 4)); }
;                     else { const u32x4 b4 = rb[ai][m][bj];
;                         b0 = (f32x4){__uint_as_float(b4.x << 16), __uint_as_float(b4.x & 0xFFFF0000u), __uint_as_float(b4.y << 16), __uint_as_float(b4.y & 0xFFFF0000u)};
;                         b1 = (f32x4){__uint_as_float(b4.z << 16), __uint_as_float(b4.z & 0xFFFF0000u), __uint_as_float(b4.w << 16), __uint_as_float(b4.w & 0xFFFF0000u)}; }
;                     const f32x4 o0 = b0 + acc[ai][bj][m][0], o1 = b1 + acc[ai][bj][m][1];
;                     if (out32) {
;                         if (!dry) { *(f32x4*)(out32 + off + bj * HALF) = o0; *(f32x4*)(out32 + off + bj * HALF + 4) = o1; }
;                         continue; }
;                     ss += ((o0[0] * o0[0] + o0[1] * o0[1]) + (o0[2] * o0[2] + o0[3] * o0[3])) + ((o1[0] * o1[0] + o1[1] * o1[1]) + (o1[2] * o1[2] + o1[3] * o1[3]));
;                     u32x4 w; w.x = cvt_pk_bf16(o0[0], o0[1]); w.y = cvt_pk_bf16(o0[2], o0[3]); w.z = cvt_pk_bf16(o1[0], o1[1]); w.w = cvt_pk_bf16(o1[2], o1[3]);
;                     if (!dry) st16_wt(xb + off + bj * HALF, w); }
.LBB0_2265:
	s_mov_b64 s[0:1], 0xb0
	v_lshl_add_u64 v[18:19], v[210:211], 0, s[0:1]
	v_lshlrev_b64 v[20:21], 10, v[18:19]
	v_lshl_add_u64 v[20:21], v[20:21], 0, v[208:209]
	v_lshlrev_b32_e32 v22, 16, v78
	v_and_b32_e32 v23, 0xffff0000, v78
	v_lshlrev_b32_e32 v24, 16, v79
	v_and_b32_e32 v25, 0xffff0000, v79
	v_lshlrev_b32_e32 v26, 16, v80
	v_and_b32_e32 v27, 0xffff0000, v80
	v_lshlrev_b32_e32 v28, 16, v81
	v_and_b32_e32 v29, 0xffff0000, v81
	v_pk_add_f32 v[16:17], v[16:17], v[24:25]
	v_pk_add_f32 v[14:15], v[14:15], v[22:23]
	v_pk_add_f32 v[12:13], v[12:13], v[28:29]
	v_pk_add_f32 v[10:11], v[10:11], v[26:27]
	s_mov_b64 s[36:37], -1
	s_and_b64 vcc, exec, s[10:11]
	v_lshl_add_u64 v[22:23], v[20:21], 2, s[18:19]
	s_cbranch_vccnz .LBB0_2267
	s_mov_b64 s[36:37], 0
	global_store_dwordx4 v[22:23], v[14:17], off sc1
	global_store_dwordx4 v[22:23], v[10:13], off offset:16 sc1

; __device__ __forceinline__ void st16_wt(void* p, u32x4 v) { asm volatile("global_store_dwordx4 %0, %1, off sc1\n\ts_nop 1" :: "v"(p), "v"(v) : "memory"); }
; __device__ __forceinline__ unsigned cvt_pk_bf16(float lo, float hi) { unsigned r; asm volatile("v_cvt_pk_bf16_f32 %0, %1, %2" : "=v"(r) : "v"(lo), "v"(hi)); return r; }
;     __device__ __forceinline__ void operator()(const Acc& acc, const Unit& u, int wr, int wc, int fr, int fq, const LAS float* tab) const {
;     ...
;                 for (int bj = 0; bj < 2; ++bj) { f32x4 b0, b1;
;                     if (base32) { b0 = __builtin_nontemporal_load((const f32x4*)(base32 + off + bj * HALF)); b1 = __builtin_nontemporal_load((const f32x4*)(base32 + off + bj * HALF + 4)); }
;                     else { const u32x4 b4 = rb[ai][m][bj];
;                         b0 = (f32x4){__uint_as_float(b4.x << 16), __uint_as_float(b4.x & 0xFFFF0000u), __uint_as_float(b4.y << 16), __uint_as_float(b4.y & 0xFFFF0000u)};
;                         b1 = (f32x4){__uint_as_float(b4.z << 16), __uint_as_float(b4.z & 0xFFFF0000u), __uint_as_float(b4.w << 16), __uint_as_float(b4.w & 0xFFFF0000u)}; }
;                     const f32x4 o0 = b0 + acc[ai][bj][m][0], o1 = b1 + acc[ai][bj][m][1];
;                     if (out32) {
;                         if (!dry) { *(f32x4*)(out32 + off + bj * HALF) = o0; *(f32x4*)(out32 + off + bj * HALF + 4) = o1; }
;                         continue; }
;                     ss += ((o0[0] * o0[0] + o0[1] * o0[1]) + (o0[2] * o0[2] + o0[3] * o0[3])) + ((o1[0] * o1[0] + o1[1] * o1[1]) + (o1[2] * o1[2] + o1[3] * o1[3]));
;                     u32x4 w; w.x = cvt_pk_bf16(o0[0], o0[1]); w.y = cvt_pk_bf16(o0[2], o0[3]); w.z = cvt_pk_bf16(o1[0], o1[1]); w.w = cvt_pk_bf16(o1[2], o1[3]);
;                     if (!dry) st16_wt(xb + off + bj * HALF, w); }
.LBB0_2269:
	v_lshlrev_b32_e32 v10, 16, v66
	v_and_b32_e32 v11, 0xffff0000, v66
	v_lshlrev_b32_e32 v12, 16, v67
	v_and_b32_e32 v13, 0xffff0000, v67
	v_lshlrev_b32_e32 v14, 16, v68
	v_and_b32_e32 v15, 0xffff0000, v68
	v_lshlrev_b32_e32 v16, 16, v69
	v_and_b32_e32 v17, 0xffff0000, v69
	v_pk_add_f32 v[8:9], v[8:9], v[12:13]
	v_pk_add_f32 v[6:7], v[6:7], v[10:11]
	v_pk_add_f32 v[4:5], v[4:5], v[16:17]
	v_pk_add_f32 v[2:3], v[2:3], v[14:15]
	s_and_b64 vcc, exec, s[10:11]
	s_mov_b64 s[10:11], -1
	s_cbranch_vccnz .LBB0_2273
	global_store_dwordx4 v[22:23], v[6:9], off offset:512 sc1
	global_store_dwordx4 v[22:23], v[2:5], off offset:528 sc1
	s_cbranch_execz .LBB0_2274

; __device__ __forceinline__ void st16_wt(void* p, u32x4 v) { asm volatile("global_store_dwordx4 %0, %1, off sc1\n\ts_nop 1" :: "v"(p), "v"(v) : "memory"); }
; __device__ __forceinline__ unsigned cvt_pk_bf16(float lo, float hi) { unsigned r; asm volatile("v_cvt_pk_bf16_f32 %0, %1, %2" : "=v"(r) : "v"(lo), "v"(hi)); return r; }
; __device__ __forceinline__ float sum_rows4(float v) {
;     const auto a = __builtin_amdgcn_permlane16_swap(__float_as_uint(v), __float_as_uint(v), false, false); const float s = __uint_as_float(a[0]) + __uint_as_float(a[1]);
;     const auto b = __builtin_amdgcn_permlane32_swap(__float_as_uint(s), __float_as_uint(s), false, false); return __uint_as_float(b[0]) + __uint_as_float(b[1]);
;     __device__ __forceinline__ void operator()(const Acc& acc, const Unit& u, int wr, int wc, int fr, int fq, const LAS float* tab) const {
;     ...
;                     ss += ((o0[0] * o0[0] + o0[1] * o0[1]) + (o0[2] * o0[2] + o0[3] * o0[3])) + ((o1[0] * o1[0] + o1[1] * o1[1]) + (o1[2] * o1[2] + o1[3] * o1[3]));
;                     u32x4 w; w.x = cvt_pk_bf16(o0[0], o0[1]); w.y = cvt_pk_bf16(o0[2], o0[3]); w.z = cvt_pk_bf16(o1[0], o1[1]); w.w = cvt_pk_bf16(o1[2], o1[3]);
;                     if (!dry) st16_wt(xb + off + bj * HALF, w); }
;                 if (out32) continue;
;                 ss = sum_rows4(ss);
;                 if (fq == 0 && !dry) ssp[row * 16 + u.pn * 4 + wc] = ss;
.LBB0_2275:
	v_mov_b32_e32 v2, v24
	s_nop 1
	v_permlane16_swap_b32_e32 v24, v2
	v_add_f32_e32 v2, v24, v2
	v_mov_b32_e32 v3, v2
	s_nop 1
	v_permlane32_swap_b32_e32 v2, v3
	s_and_saveexec_b64 s[10:11], s[6:7]
	s_cbranch_execz .LBB0_2277
	v_add_f32_e32 v4, v2, v3
	v_lshlrev_b64 v[2:3], 6, v[18:19]
	v_lshl_add_u64 v[2:3], s[34:35], 0, v[2:3]
	global_store_dword v[2:3], v4, off sc1

; __device__ __forceinline__ unsigned xb_ld(unsigned* p)              { return __hip_atomic_load(p, __ATOMIC_RELAXED, __HIP_MEMORY_SCOPE_AGENT); }
; __device__ __forceinline__ unsigned xb_add(unsigned* p, unsigned v) { return __hip_atomic_fetch_add(p, v, __ATOMIC_RELAXED, __HIP_MEMORY_SCOPE_AGENT); }
; #define XB_SPIN(cond, bar) do { unsigned _sp = 0; while (cond) { __builtin_amdgcn_s_sleep(1); \
;     if ((++_sp & 255u) == 0u) { if (xb_ld(&(bar)[XB_TMO])) break; if (_sp > XB_SPIN_CAP) { atomicAdd(&(bar)[XB_TMO], 1u); break; } } } } while (0)
; __device__ __forceinline__ void xcd_barrier_impl(const XcdBarrier& b, bool leader) {
;     ...
;         const unsigned old = xb_add(&bar[XB_XSUB(b.x)], 1u);
;         const unsigned gen = old / nloc;
;         if (old + 1u == (gen + 1u) * nloc) {
;             __builtin_amdgcn_fence(__ATOMIC_RELEASE, "agent");
;             asm volatile("s_waitcnt vmcnt(0)" ::: "memory");
;             const unsigned og = xb_add(&bar[XB_TOP], 1u);
;             const unsigned tg = og / nx;
;             if (og + 1u != (tg + 1u) * nx) XB_SPIN(xb_ld(&bar[XB_TOP]) < (tg + 1u) * nx, bar);
.LBB0_2317:
	s_mov_b64 s[10:11], exec
	s_waitcnt lgkmcnt(0)
	s_waitcnt vmcnt(0)
	v_mbcnt_lo_u32_b32 v2, s10, 0
	s_add_u32 s8, s6, 0x7400
	v_mbcnt_hi_u32_b32 v2, s11, v2
	s_addc_u32 s9, s7, 0
	v_cmp_eq_u32_e32 vcc, 0, v2
	s_and_saveexec_b64 s[12:13], vcc
	s_cbranch_execz .LBB0_2319
	s_bcnt1_i32_b64 s0, s[10:11]
	v_mov_b32_e32 v3, s0
	global_atomic_add v3, v1, v3, s[8:9] sc0
